# speedup vs baseline: 1.3157x; 1.0174x over previous
.LBB0_65:
	s_or_b64 exec, exec, s[12:13]
	v_mov_b32_e32 v0, 0x20000
	s_waitcnt lgkmcnt(0)
	s_barrier
	ds_read_b96 v[186:188], v0
	v_lshlrev_b32_e32 v0, 10, v193
	s_load_dwordx4 s[12:15], s[0:1], 0x8
	v_and_b32_e32 v0, 0xc00, v0
	v_lshlrev_b32_e32 v1, 1, v193
	s_waitcnt lgkmcnt(0)
	v_readfirstlane_b32 s18, v188
	s_lshl_b32 s2, s18, 5
	v_add_u32_e32 v0, s2, v0
	v_bfe_u32 v109, v193, 4, 2
	v_and_or_b32 v0, v1, 24, v0
	s_lshr_b32 s3, s3, 6
	v_lshlrev_b32_e32 v217, 3, v109
	v_ashrrev_i32_e32 v1, 31, v0
	v_lshl_or_b32 v200, s3, 8, v217
	v_lshlrev_b64 v[4:5], 2, v[0:1]
	v_mov_b32_e32 v201, 0
	v_lshl_add_u64 v[6:7], s[14:15], 0, v[4:5]
	v_lshlrev_b64 v[0:1], 14, v[200:201]
	v_lshl_add_u64 v[0:1], v[6:7], 0, v[0:1]
	global_load_dwordx4 v[8:11], v[0:1], off offset:16
	global_load_dwordx4 v[12:15], v[0:1], off
	v_or_b32_e32 v0, 1, v200
	v_mov_b32_e32 v1, v201
	v_lshlrev_b64 v[0:1], 14, v[0:1]
	v_lshl_add_u64 v[0:1], v[6:7], 0, v[0:1]
	global_load_dwordx4 v[16:19], v[0:1], off offset:16
	global_load_dwordx4 v[20:23], v[0:1], off
	v_or_b32_e32 v0, 2, v200
	v_mov_b32_e32 v1, v201
	v_lshlrev_b64 v[0:1], 14, v[0:1]
	v_lshl_add_u64 v[0:1], v[6:7], 0, v[0:1]
	global_load_dwordx4 v[24:27], v[0:1], off offset:16
	global_load_dwordx4 v[28:31], v[0:1], off
	v_or_b32_e32 v0, 3, v200
	v_mov_b32_e32 v1, v201
	v_lshlrev_b64 v[0:1], 14, v[0:1]
	v_lshl_add_u64 v[0:1], v[6:7], 0, v[0:1]
	global_load_dwordx4 v[32:35], v[0:1], off offset:16
	global_load_dwordx4 v[36:39], v[0:1], off
	v_or_b32_e32 v0, 4, v200
	v_mov_b32_e32 v1, v201
	v_lshlrev_b64 v[0:1], 14, v[0:1]
	v_lshl_add_u64 v[0:1], v[6:7], 0, v[0:1]
	global_load_dwordx4 v[40:43], v[0:1], off offset:16
	global_load_dwordx4 v[44:47], v[0:1], off
	v_or_b32_e32 v0, 5, v200
	v_mov_b32_e32 v1, v201
	v_lshlrev_b64 v[0:1], 14, v[0:1]
	v_lshl_add_u64 v[0:1], v[6:7], 0, v[0:1]
	global_load_dwordx4 v[48:51], v[0:1], off offset:16
	global_load_dwordx4 v[52:55], v[0:1], off
	v_or_b32_e32 v0, 6, v200
	v_mov_b32_e32 v1, v201
	v_lshlrev_b64 v[0:1], 14, v[0:1]
	v_lshl_add_u64 v[0:1], v[6:7], 0, v[0:1]
	global_load_dwordx4 v[56:59], v[0:1], off offset:16
	global_load_dwordx4 v[60:63], v[0:1], off
	v_or_b32_e32 v0, 7, v200
	v_mov_b32_e32 v1, v201
	v_lshlrev_b64 v[0:1], 14, v[0:1]
	v_lshl_add_u64 v[0:1], v[6:7], 0, v[0:1]
	global_load_dwordx4 v[64:67], v[0:1], off offset:16
	global_load_dwordx4 v[68:71], v[0:1], off
	v_mov_b32_e32 v1, v201
	s_lshl_b32 s14, s3, 7
	v_and_b32_e32 v198, 63, v193
	v_lshlrev_b32_e32 v108, 4, v198
	v_lshl_or_b32 v95, s3, 15, v108
	s_lshl_b32 s0, s3, 11
	v_bfe_u32 v207, v193, 3, 3
	s_lshl_b32 s20, s3, 3
	v_or_b32_e32 v208, s20, v207
	v_readfirstlane_b32 s19, v187
	v_and_b32_e32 v150, 7, v193
	s_mov_b32 s15, 0
	v_or_b32_e32 v198, s0, v198
	s_mov_b32 s24, s15
	s_mov_b32 s25, s15
	s_mov_b32 s26, s15
	s_mov_b32 s27, s15
	v_and_b32_e32 v220, 15, v193
	s_lshl_b32 s22, s18, 2
	s_add_i32 s22, s22, s3
	s_lshl_b32 s21, s3, 12
	s_and_b32 s3, s22, 7
	s_ashr_i32 s23, s22, 3
	s_and_b32 s9, s9, 0xffff
	s_add_i32 s23, s23, 16
	v_mov_b32_e32 v202, v201
	v_mov_b32_e32 v203, v201
	s_mov_b32 s11, 0x20000
	s_mov_b32 s10, 0x40000
	s_waitcnt vmcnt(12)
	v_cvt_pk_f16_f32 v231, v12, v20
	v_accvgpr_write_b32 a0, v231
	s_waitcnt vmcnt(8)
	v_cvt_pk_f16_f32 v230, v28, v36
	v_accvgpr_write_b32 a1, v230
	s_waitcnt vmcnt(4)
	v_cvt_pk_f16_f32 v229, v44, v52
	v_accvgpr_write_b32 a2, v229
	s_waitcnt vmcnt(1)
	v_cvt_pk_f16_f32 v0, v56, v64
	v_accvgpr_write_b32 a131, v0
	v_cvt_pk_f16_f32 v0, v40, v48
	v_accvgpr_write_b32 a130, v0
	v_cvt_pk_f16_f32 v0, v24, v32
	v_accvgpr_write_b32 a129, v0
	v_cvt_pk_f16_f32 v0, v8, v16
	v_accvgpr_write_b32 a128, v0
	s_waitcnt vmcnt(0)
	v_cvt_pk_f16_f32 v0, v61, v69
	v_accvgpr_write_b32 a35, v0
	v_cvt_pk_f16_f32 v0, v45, v53
	v_accvgpr_write_b32 a34, v0
	v_cvt_pk_f16_f32 v0, v29, v37
	v_accvgpr_write_b32 a33, v0
	v_cvt_pk_f16_f32 v0, v13, v21
	v_accvgpr_write_b32 a32, v0
	v_cvt_pk_f16_f32 v0, v57, v65
	v_accvgpr_write_b32 a163, v0
	v_cvt_pk_f16_f32 v0, v41, v49
	v_accvgpr_write_b32 a162, v0
	v_cvt_pk_f16_f32 v0, v25, v33
	v_accvgpr_write_b32 a161, v0
	v_cvt_pk_f16_f32 v0, v9, v17
	v_accvgpr_write_b32 a160, v0
	v_cvt_pk_f16_f32 v0, v62, v70
	v_accvgpr_write_b32 a67, v0
	v_cvt_pk_f16_f32 v0, v46, v54
	v_accvgpr_write_b32 a66, v0
	v_cvt_pk_f16_f32 v0, v30, v38
	v_accvgpr_write_b32 a65, v0
	v_cvt_pk_f16_f32 v0, v14, v22
	v_accvgpr_write_b32 a64, v0
	v_cvt_pk_f16_f32 v0, v58, v66
	v_accvgpr_write_b32 a195, v0
	v_cvt_pk_f16_f32 v0, v42, v50
	v_accvgpr_write_b32 a194, v0
	v_cvt_pk_f16_f32 v0, v26, v34
	v_accvgpr_write_b32 a193, v0
	v_cvt_pk_f16_f32 v0, v10, v18
	v_accvgpr_write_b32 a192, v0
	v_cvt_pk_f16_f32 v0, v63, v71
	v_accvgpr_write_b32 a99, v0
	v_cvt_pk_f16_f32 v0, v47, v55
	v_accvgpr_write_b32 a98, v0
	v_cvt_pk_f16_f32 v0, v31, v39
	v_accvgpr_write_b32 a97, v0
	v_cvt_pk_f16_f32 v0, v15, v23
	v_accvgpr_write_b32 a96, v0
	v_cvt_pk_f16_f32 v0, v59, v67
	v_accvgpr_write_b32 a227, v0
	v_cvt_pk_f16_f32 v0, v43, v51
	v_accvgpr_write_b32 a226, v0
	v_cvt_pk_f16_f32 v0, v27, v35
	v_accvgpr_write_b32 a225, v0
	v_cvt_pk_f16_f32 v0, v11, v19
	v_accvgpr_write_b32 a224, v0
	v_or_b32_e32 v0, 32, v200
	v_lshlrev_b64 v[0:1], 14, v[0:1]
	v_lshl_add_u64 v[0:1], v[6:7], 0, v[0:1]
	global_load_dwordx4 v[8:11], v[0:1], off offset:16
	global_load_dwordx4 v[12:15], v[0:1], off
	v_or_b32_e32 v0, 33, v200
	v_mov_b32_e32 v1, v201
	v_lshlrev_b64 v[0:1], 14, v[0:1]
	v_lshl_add_u64 v[0:1], v[6:7], 0, v[0:1]
	global_load_dwordx4 v[16:19], v[0:1], off offset:16
	global_load_dwordx4 v[20:23], v[0:1], off
	v_or_b32_e32 v0, 34, v200
	v_mov_b32_e32 v1, v201
	v_lshlrev_b64 v[0:1], 14, v[0:1]
	v_lshl_add_u64 v[0:1], v[6:7], 0, v[0:1]
	global_load_dwordx4 v[24:27], v[0:1], off offset:16
	global_load_dwordx4 v[28:31], v[0:1], off
	v_or_b32_e32 v0, 35, v200
	v_mov_b32_e32 v1, v201
	v_lshlrev_b64 v[0:1], 14, v[0:1]
	v_lshl_add_u64 v[0:1], v[6:7], 0, v[0:1]
	global_load_dwordx4 v[32:35], v[0:1], off offset:16
	global_load_dwordx4 v[36:39], v[0:1], off
	v_or_b32_e32 v0, 36, v200
	v_mov_b32_e32 v1, v201
	v_lshlrev_b64 v[0:1], 14, v[0:1]
	v_lshl_add_u64 v[0:1], v[6:7], 0, v[0:1]
	global_load_dwordx4 v[40:43], v[0:1], off offset:16
	global_load_dwordx4 v[44:47], v[0:1], off
	v_or_b32_e32 v0, 37, v200
	v_mov_b32_e32 v1, v201
	v_lshlrev_b64 v[0:1], 14, v[0:1]
	v_lshl_add_u64 v[0:1], v[6:7], 0, v[0:1]
	global_load_dwordx4 v[48:51], v[0:1], off offset:16
	global_load_dwordx4 v[52:55], v[0:1], off
	v_or_b32_e32 v0, 38, v200
	v_mov_b32_e32 v1, v201
	v_lshlrev_b64 v[0:1], 14, v[0:1]
	v_lshl_add_u64 v[0:1], v[6:7], 0, v[0:1]
	v_cvt_pk_f16_f32 v228, v60, v68
	global_load_dwordx4 v[56:59], v[0:1], off offset:16
	global_load_dwordx4 v[60:63], v[0:1], off
	v_or_b32_e32 v0, 39, v200
	v_mov_b32_e32 v1, v201
	v_lshlrev_b64 v[0:1], 14, v[0:1]
	v_lshl_add_u64 v[0:1], v[6:7], 0, v[0:1]
	global_load_dwordx4 v[64:67], v[0:1], off offset:16
	global_load_dwordx4 v[68:71], v[0:1], off
	v_mov_b32_e32 v1, v201
	v_accvgpr_write_b32 a3, v228
	s_waitcnt vmcnt(12)
	v_cvt_pk_f16_f32 v206, v12, v20
	v_accvgpr_write_b32 a4, v206
	s_waitcnt vmcnt(8)
	v_cvt_pk_f16_f32 v197, v28, v36
	v_accvgpr_write_b32 a5, v197
	s_waitcnt vmcnt(4)
	v_cvt_pk_f16_f32 v199, v44, v52
	v_accvgpr_write_b32 a6, v199
	s_waitcnt vmcnt(1)
	v_cvt_pk_f16_f32 v0, v56, v64
	v_accvgpr_write_b32 a135, v0
	v_cvt_pk_f16_f32 v0, v40, v48
	v_accvgpr_write_b32 a134, v0
	v_cvt_pk_f16_f32 v0, v24, v32
	v_accvgpr_write_b32 a133, v0
	v_cvt_pk_f16_f32 v0, v8, v16
	v_accvgpr_write_b32 a132, v0
	s_waitcnt vmcnt(0)
	v_cvt_pk_f16_f32 v0, v61, v69
	v_accvgpr_write_b32 a39, v0
	v_cvt_pk_f16_f32 v0, v45, v53
	v_accvgpr_write_b32 a38, v0
	v_cvt_pk_f16_f32 v0, v29, v37
	v_accvgpr_write_b32 a37, v0
	v_cvt_pk_f16_f32 v0, v13, v21
	v_accvgpr_write_b32 a36, v0
	v_cvt_pk_f16_f32 v0, v57, v65
	v_accvgpr_write_b32 a167, v0
	v_cvt_pk_f16_f32 v0, v41, v49
	v_accvgpr_write_b32 a166, v0
	v_cvt_pk_f16_f32 v0, v25, v33
	v_accvgpr_write_b32 a165, v0
	v_cvt_pk_f16_f32 v0, v9, v17
	v_accvgpr_write_b32 a164, v0
	v_cvt_pk_f16_f32 v0, v62, v70
	v_accvgpr_write_b32 a71, v0
	v_cvt_pk_f16_f32 v0, v46, v54
	v_accvgpr_write_b32 a70, v0
	v_cvt_pk_f16_f32 v0, v30, v38
	v_accvgpr_write_b32 a69, v0
	v_cvt_pk_f16_f32 v0, v14, v22
	v_accvgpr_write_b32 a68, v0
	v_cvt_pk_f16_f32 v0, v58, v66
	v_accvgpr_write_b32 a199, v0
	v_cvt_pk_f16_f32 v0, v42, v50
	v_accvgpr_write_b32 a198, v0
	v_cvt_pk_f16_f32 v0, v26, v34
	v_accvgpr_write_b32 a197, v0
	v_cvt_pk_f16_f32 v0, v10, v18
	v_accvgpr_write_b32 a196, v0
	v_cvt_pk_f16_f32 v0, v63, v71
	v_accvgpr_write_b32 a103, v0
	v_cvt_pk_f16_f32 v0, v47, v55
	v_accvgpr_write_b32 a102, v0
	v_cvt_pk_f16_f32 v0, v31, v39
	v_accvgpr_write_b32 a101, v0
	v_cvt_pk_f16_f32 v0, v15, v23
	v_accvgpr_write_b32 a100, v0
	v_cvt_pk_f16_f32 v0, v59, v67
	v_accvgpr_write_b32 a231, v0
	v_cvt_pk_f16_f32 v0, v43, v51
	v_accvgpr_write_b32 a230, v0
	v_cvt_pk_f16_f32 v0, v27, v35
	v_accvgpr_write_b32 a229, v0
	v_cvt_pk_f16_f32 v0, v11, v19
	v_accvgpr_write_b32 a228, v0
	v_or_b32_e32 v0, 64, v200
	v_lshlrev_b64 v[0:1], 14, v[0:1]
	v_lshl_add_u64 v[0:1], v[6:7], 0, v[0:1]
	global_load_dwordx4 v[8:11], v[0:1], off offset:16
	global_load_dwordx4 v[12:15], v[0:1], off
	v_or_b32_e32 v0, 0x41, v200
	v_mov_b32_e32 v1, v201
	v_lshlrev_b64 v[0:1], 14, v[0:1]
	v_lshl_add_u64 v[0:1], v[6:7], 0, v[0:1]
	global_load_dwordx4 v[16:19], v[0:1], off offset:16
	global_load_dwordx4 v[20:23], v[0:1], off
	v_or_b32_e32 v0, 0x42, v200
	v_mov_b32_e32 v1, v201
	v_lshlrev_b64 v[0:1], 14, v[0:1]
	v_lshl_add_u64 v[0:1], v[6:7], 0, v[0:1]
	global_load_dwordx4 v[24:27], v[0:1], off offset:16
	global_load_dwordx4 v[28:31], v[0:1], off
	v_or_b32_e32 v0, 0x43, v200
	v_mov_b32_e32 v1, v201
	v_lshlrev_b64 v[0:1], 14, v[0:1]
	v_lshl_add_u64 v[0:1], v[6:7], 0, v[0:1]
	global_load_dwordx4 v[32:35], v[0:1], off offset:16
	global_load_dwordx4 v[36:39], v[0:1], off
	v_or_b32_e32 v0, 0x44, v200
	v_mov_b32_e32 v1, v201
	v_lshlrev_b64 v[0:1], 14, v[0:1]
	v_lshl_add_u64 v[0:1], v[6:7], 0, v[0:1]
	global_load_dwordx4 v[40:43], v[0:1], off offset:16
	global_load_dwordx4 v[44:47], v[0:1], off
	v_or_b32_e32 v0, 0x45, v200
	v_mov_b32_e32 v1, v201
	v_lshlrev_b64 v[0:1], 14, v[0:1]
	v_lshl_add_u64 v[0:1], v[6:7], 0, v[0:1]
	global_load_dwordx4 v[48:51], v[0:1], off offset:16
	global_load_dwordx4 v[52:55], v[0:1], off
	v_or_b32_e32 v0, 0x46, v200
	v_mov_b32_e32 v1, v201
	v_lshlrev_b64 v[0:1], 14, v[0:1]
	v_lshl_add_u64 v[0:1], v[6:7], 0, v[0:1]
	v_cvt_pk_f16_f32 v205, v60, v68
	global_load_dwordx4 v[56:59], v[0:1], off offset:16
	global_load_dwordx4 v[60:63], v[0:1], off
	v_or_b32_e32 v0, 0x47, v200
	v_mov_b32_e32 v1, v201
	v_lshlrev_b64 v[0:1], 14, v[0:1]
	v_lshl_add_u64 v[0:1], v[6:7], 0, v[0:1]
	global_load_dwordx4 v[64:67], v[0:1], off offset:16
	global_load_dwordx4 v[68:71], v[0:1], off
	v_mov_b32_e32 v1, v201
	v_accvgpr_write_b32 a7, v205
	s_waitcnt vmcnt(12)
	v_cvt_pk_f16_f32 v155, v12, v20
	v_accvgpr_write_b32 a8, v155
	s_waitcnt vmcnt(8)
	v_cvt_pk_f16_f32 v156, v28, v36
	v_accvgpr_write_b32 a9, v156
	s_waitcnt vmcnt(4)
	v_cvt_pk_f16_f32 v157, v44, v52
	v_accvgpr_write_b32 a10, v157
	s_waitcnt vmcnt(1)
	v_cvt_pk_f16_f32 v0, v56, v64
	v_accvgpr_write_b32 a139, v0
	v_cvt_pk_f16_f32 v0, v40, v48
	v_accvgpr_write_b32 a138, v0
	v_cvt_pk_f16_f32 v0, v24, v32
	v_accvgpr_write_b32 a137, v0
	v_cvt_pk_f16_f32 v0, v8, v16
	v_accvgpr_write_b32 a136, v0
	s_waitcnt vmcnt(0)
	v_cvt_pk_f16_f32 v0, v61, v69
	v_accvgpr_write_b32 a43, v0
	v_cvt_pk_f16_f32 v0, v45, v53
	v_accvgpr_write_b32 a42, v0
	v_cvt_pk_f16_f32 v0, v29, v37
	v_accvgpr_write_b32 a41, v0
	v_cvt_pk_f16_f32 v0, v13, v21
	v_accvgpr_write_b32 a40, v0
	v_cvt_pk_f16_f32 v0, v57, v65
	v_accvgpr_write_b32 a171, v0
	v_cvt_pk_f16_f32 v0, v41, v49
	v_accvgpr_write_b32 a170, v0
	v_cvt_pk_f16_f32 v0, v25, v33
	v_accvgpr_write_b32 a169, v0
	v_cvt_pk_f16_f32 v0, v9, v17
	v_accvgpr_write_b32 a168, v0
	v_cvt_pk_f16_f32 v0, v62, v70
	v_accvgpr_write_b32 a75, v0
	v_cvt_pk_f16_f32 v0, v46, v54
	v_accvgpr_write_b32 a74, v0
	v_cvt_pk_f16_f32 v0, v30, v38
	v_accvgpr_write_b32 a73, v0
	v_cvt_pk_f16_f32 v0, v14, v22
	v_accvgpr_write_b32 a72, v0
	v_cvt_pk_f16_f32 v0, v58, v66
	v_accvgpr_write_b32 a203, v0
	v_cvt_pk_f16_f32 v0, v42, v50
	v_accvgpr_write_b32 a202, v0
	v_cvt_pk_f16_f32 v0, v26, v34
	v_accvgpr_write_b32 a201, v0
	v_cvt_pk_f16_f32 v0, v10, v18
	v_accvgpr_write_b32 a200, v0
	v_cvt_pk_f16_f32 v0, v63, v71
	v_accvgpr_write_b32 a107, v0
	v_cvt_pk_f16_f32 v0, v47, v55
	v_accvgpr_write_b32 a106, v0
	v_cvt_pk_f16_f32 v0, v31, v39
	v_accvgpr_write_b32 a105, v0
	v_cvt_pk_f16_f32 v0, v15, v23
	v_accvgpr_write_b32 a104, v0
	v_cvt_pk_f16_f32 v0, v59, v67
	v_accvgpr_write_b32 a235, v0
	v_cvt_pk_f16_f32 v0, v43, v51
	v_accvgpr_write_b32 a234, v0
	v_cvt_pk_f16_f32 v0, v27, v35
	v_accvgpr_write_b32 a233, v0
	v_cvt_pk_f16_f32 v0, v11, v19
	v_accvgpr_write_b32 a232, v0
	v_or_b32_e32 v0, 0x60, v200
	v_lshlrev_b64 v[0:1], 14, v[0:1]
	v_lshl_add_u64 v[0:1], v[6:7], 0, v[0:1]
	global_load_dwordx4 v[8:11], v[0:1], off offset:16
	global_load_dwordx4 v[12:15], v[0:1], off
	v_or_b32_e32 v0, 0x61, v200
	v_mov_b32_e32 v1, v201
	v_lshlrev_b64 v[0:1], 14, v[0:1]
	v_lshl_add_u64 v[0:1], v[6:7], 0, v[0:1]
	global_load_dwordx4 v[16:19], v[0:1], off offset:16
	global_load_dwordx4 v[20:23], v[0:1], off
	v_or_b32_e32 v0, 0x62, v200
	v_mov_b32_e32 v1, v201
	v_lshlrev_b64 v[0:1], 14, v[0:1]
	v_lshl_add_u64 v[0:1], v[6:7], 0, v[0:1]
	global_load_dwordx4 v[24:27], v[0:1], off offset:16
	global_load_dwordx4 v[28:31], v[0:1], off
	v_or_b32_e32 v0, 0x63, v200
	v_mov_b32_e32 v1, v201
	v_lshlrev_b64 v[0:1], 14, v[0:1]
	v_lshl_add_u64 v[0:1], v[6:7], 0, v[0:1]
	global_load_dwordx4 v[32:35], v[0:1], off offset:16
	global_load_dwordx4 v[36:39], v[0:1], off
	v_or_b32_e32 v0, 0x64, v200
	v_mov_b32_e32 v1, v201
	v_lshlrev_b64 v[0:1], 14, v[0:1]
	v_lshl_add_u64 v[0:1], v[6:7], 0, v[0:1]
	global_load_dwordx4 v[40:43], v[0:1], off offset:16
	global_load_dwordx4 v[44:47], v[0:1], off
	v_or_b32_e32 v0, 0x65, v200
	v_mov_b32_e32 v1, v201
	v_lshlrev_b64 v[0:1], 14, v[0:1]
	v_lshl_add_u64 v[0:1], v[6:7], 0, v[0:1]
	global_load_dwordx4 v[48:51], v[0:1], off offset:16
	global_load_dwordx4 v[52:55], v[0:1], off
	v_or_b32_e32 v0, 0x66, v200
	v_mov_b32_e32 v1, v201
	v_lshlrev_b64 v[0:1], 14, v[0:1]
	v_lshl_add_u64 v[0:1], v[6:7], 0, v[0:1]
	v_cvt_pk_f16_f32 v158, v60, v68
	global_load_dwordx4 v[56:59], v[0:1], off offset:16
	global_load_dwordx4 v[60:63], v[0:1], off
	v_or_b32_e32 v0, 0x67, v200
	v_mov_b32_e32 v1, v201
	v_lshlrev_b64 v[0:1], 14, v[0:1]
	v_lshl_add_u64 v[0:1], v[6:7], 0, v[0:1]
	global_load_dwordx4 v[64:67], v[0:1], off offset:16
	global_load_dwordx4 v[68:71], v[0:1], off
	v_mov_b32_e32 v1, v201
	v_accvgpr_write_b32 a11, v158
	s_waitcnt vmcnt(12)
	v_cvt_pk_f16_f32 v122, v12, v20
	v_accvgpr_write_b32 a12, v122
	s_waitcnt vmcnt(8)
	v_cvt_pk_f16_f32 v123, v28, v36
	v_accvgpr_write_b32 a13, v123
	s_waitcnt vmcnt(4)
	v_cvt_pk_f16_f32 v124, v44, v52
	v_accvgpr_write_b32 a14, v124
	s_waitcnt vmcnt(1)
	v_cvt_pk_f16_f32 v0, v56, v64
	v_accvgpr_write_b32 a143, v0
	v_cvt_pk_f16_f32 v0, v40, v48
	v_accvgpr_write_b32 a142, v0
	v_cvt_pk_f16_f32 v0, v24, v32
	v_accvgpr_write_b32 a141, v0
	v_cvt_pk_f16_f32 v0, v8, v16
	v_accvgpr_write_b32 a140, v0
	s_waitcnt vmcnt(0)
	v_cvt_pk_f16_f32 v0, v61, v69
	v_accvgpr_write_b32 a47, v0
	v_cvt_pk_f16_f32 v0, v45, v53
	v_accvgpr_write_b32 a46, v0
	v_cvt_pk_f16_f32 v0, v29, v37
	v_accvgpr_write_b32 a45, v0
	v_cvt_pk_f16_f32 v0, v13, v21
	v_accvgpr_write_b32 a44, v0
	v_cvt_pk_f16_f32 v0, v57, v65
	v_accvgpr_write_b32 a175, v0
	v_cvt_pk_f16_f32 v0, v41, v49
	v_accvgpr_write_b32 a174, v0
	v_cvt_pk_f16_f32 v0, v25, v33
	v_accvgpr_write_b32 a173, v0
	v_cvt_pk_f16_f32 v0, v9, v17
	v_accvgpr_write_b32 a172, v0
	v_cvt_pk_f16_f32 v0, v62, v70
	v_accvgpr_write_b32 a79, v0
	v_cvt_pk_f16_f32 v0, v46, v54
	v_accvgpr_write_b32 a78, v0
	v_cvt_pk_f16_f32 v0, v30, v38
	v_accvgpr_write_b32 a77, v0
	v_cvt_pk_f16_f32 v0, v14, v22
	v_accvgpr_write_b32 a76, v0
	v_cvt_pk_f16_f32 v0, v58, v66
	v_accvgpr_write_b32 a207, v0
	v_cvt_pk_f16_f32 v0, v42, v50
	v_accvgpr_write_b32 a206, v0
	v_cvt_pk_f16_f32 v0, v26, v34
	v_accvgpr_write_b32 a205, v0
	v_cvt_pk_f16_f32 v0, v10, v18
	v_accvgpr_write_b32 a204, v0
	v_cvt_pk_f16_f32 v0, v63, v71
	v_accvgpr_write_b32 a111, v0
	v_cvt_pk_f16_f32 v0, v47, v55
	v_accvgpr_write_b32 a110, v0
	v_cvt_pk_f16_f32 v0, v31, v39
	v_accvgpr_write_b32 a109, v0
	v_cvt_pk_f16_f32 v0, v15, v23
	v_accvgpr_write_b32 a108, v0
	v_cvt_pk_f16_f32 v0, v59, v67
	v_accvgpr_write_b32 a239, v0
	v_cvt_pk_f16_f32 v0, v43, v51
	v_accvgpr_write_b32 a238, v0
	v_cvt_pk_f16_f32 v0, v27, v35
	v_accvgpr_write_b32 a237, v0
	v_cvt_pk_f16_f32 v0, v11, v19
	v_accvgpr_write_b32 a236, v0
	v_or_b32_e32 v0, 0x80, v200
	v_lshlrev_b64 v[0:1], 14, v[0:1]
	v_lshl_add_u64 v[0:1], v[6:7], 0, v[0:1]
	global_load_dwordx4 v[8:11], v[0:1], off offset:16
	global_load_dwordx4 v[12:15], v[0:1], off
	v_or_b32_e32 v0, 0x81, v200
	v_mov_b32_e32 v1, v201
	v_lshlrev_b64 v[0:1], 14, v[0:1]
	v_lshl_add_u64 v[0:1], v[6:7], 0, v[0:1]
	global_load_dwordx4 v[16:19], v[0:1], off offset:16
	global_load_dwordx4 v[20:23], v[0:1], off
	v_or_b32_e32 v0, 0x82, v200
	v_mov_b32_e32 v1, v201
	v_lshlrev_b64 v[0:1], 14, v[0:1]
	v_lshl_add_u64 v[0:1], v[6:7], 0, v[0:1]
	global_load_dwordx4 v[24:27], v[0:1], off offset:16
	global_load_dwordx4 v[28:31], v[0:1], off
	v_or_b32_e32 v0, 0x83, v200
	v_mov_b32_e32 v1, v201
	v_lshlrev_b64 v[0:1], 14, v[0:1]
	v_lshl_add_u64 v[0:1], v[6:7], 0, v[0:1]
	global_load_dwordx4 v[32:35], v[0:1], off offset:16
	global_load_dwordx4 v[36:39], v[0:1], off
	v_or_b32_e32 v0, 0x84, v200
	v_mov_b32_e32 v1, v201
	v_lshlrev_b64 v[0:1], 14, v[0:1]
	v_lshl_add_u64 v[0:1], v[6:7], 0, v[0:1]
	global_load_dwordx4 v[40:43], v[0:1], off offset:16
	global_load_dwordx4 v[44:47], v[0:1], off
	v_or_b32_e32 v0, 0x85, v200
	v_mov_b32_e32 v1, v201
	v_lshlrev_b64 v[0:1], 14, v[0:1]
	v_lshl_add_u64 v[0:1], v[6:7], 0, v[0:1]
	global_load_dwordx4 v[48:51], v[0:1], off offset:16
	global_load_dwordx4 v[52:55], v[0:1], off
	v_or_b32_e32 v0, 0x86, v200
	v_mov_b32_e32 v1, v201
	v_lshlrev_b64 v[0:1], 14, v[0:1]
	v_lshl_add_u64 v[0:1], v[6:7], 0, v[0:1]
	v_cvt_pk_f16_f32 v125, v60, v68
	global_load_dwordx4 v[56:59], v[0:1], off offset:16
	global_load_dwordx4 v[60:63], v[0:1], off
	v_or_b32_e32 v0, 0x87, v200
	v_mov_b32_e32 v1, v201
	v_lshlrev_b64 v[0:1], 14, v[0:1]
	v_lshl_add_u64 v[0:1], v[6:7], 0, v[0:1]
	global_load_dwordx4 v[64:67], v[0:1], off offset:16
	global_load_dwordx4 v[68:71], v[0:1], off
	v_mov_b32_e32 v1, v201
	v_accvgpr_write_b32 a15, v125
	s_waitcnt vmcnt(12)
	v_cvt_pk_f16_f32 v114, v12, v20
	v_cvt_pk_f16_f32 v245, v13, v21
	v_cvt_pk_f16_f32 v235, v14, v22
	v_cvt_pk_f16_f32 v227, v15, v23
	v_accvgpr_write_b32 a16, v114
	v_accvgpr_write_b32 a48, v245
	v_accvgpr_write_b32 a80, v235
	v_accvgpr_write_b32 a112, v227
	s_waitcnt vmcnt(8)
	v_cvt_pk_f16_f32 v115, v28, v36
	v_cvt_pk_f16_f32 v243, v29, v37
	v_cvt_pk_f16_f32 v234, v30, v38
	v_cvt_pk_f16_f32 v226, v31, v39
	v_accvgpr_write_b32 a17, v115
	v_accvgpr_write_b32 a49, v243
	v_accvgpr_write_b32 a81, v234
	v_accvgpr_write_b32 a113, v226
	s_waitcnt vmcnt(4)
	v_cvt_pk_f16_f32 v116, v44, v52
	v_cvt_pk_f16_f32 v241, v45, v53
	v_cvt_pk_f16_f32 v233, v46, v54
	v_cvt_pk_f16_f32 v225, v47, v55
	v_accvgpr_write_b32 a18, v116
	v_accvgpr_write_b32 a50, v241
	v_accvgpr_write_b32 a82, v233
	v_accvgpr_write_b32 a114, v225
	s_waitcnt vmcnt(1)
	v_cvt_pk_f16_f32 v0, v56, v64
	v_accvgpr_write_b32 a147, v0
	v_cvt_pk_f16_f32 v0, v40, v48
	v_accvgpr_write_b32 a146, v0
	v_cvt_pk_f16_f32 v0, v24, v32
	v_accvgpr_write_b32 a145, v0
	v_cvt_pk_f16_f32 v0, v8, v16
	v_accvgpr_write_b32 a144, v0
	v_cvt_pk_f16_f32 v0, v57, v65
	v_accvgpr_write_b32 a179, v0
	v_cvt_pk_f16_f32 v0, v41, v49
	v_accvgpr_write_b32 a178, v0
	v_cvt_pk_f16_f32 v0, v25, v33
	v_accvgpr_write_b32 a177, v0
	v_cvt_pk_f16_f32 v0, v9, v17
	v_accvgpr_write_b32 a176, v0
	v_cvt_pk_f16_f32 v0, v58, v66
	v_accvgpr_write_b32 a211, v0
	v_cvt_pk_f16_f32 v0, v42, v50
	v_accvgpr_write_b32 a210, v0
	v_cvt_pk_f16_f32 v0, v26, v34
	v_accvgpr_write_b32 a209, v0
	v_cvt_pk_f16_f32 v0, v10, v18
	v_accvgpr_write_b32 a208, v0
	s_waitcnt vmcnt(0)
	v_cvt_pk_f16_f32 v0, v63, v71
	v_accvgpr_write_b32 a115, v0
	v_cvt_pk_f16_f32 v0, v59, v67
	v_accvgpr_write_b32 a243, v0
	v_cvt_pk_f16_f32 v0, v43, v51
	v_accvgpr_write_b32 a242, v0
	v_cvt_pk_f16_f32 v0, v27, v35
	v_accvgpr_write_b32 a241, v0
	v_cvt_pk_f16_f32 v0, v11, v19
	v_accvgpr_write_b32 a240, v0
	v_or_b32_e32 v0, 0xa0, v200
	v_lshlrev_b64 v[0:1], 14, v[0:1]
	v_lshl_add_u64 v[0:1], v[6:7], 0, v[0:1]
	global_load_dwordx4 v[8:11], v[0:1], off offset:16
	global_load_dwordx4 v[12:15], v[0:1], off
	v_or_b32_e32 v0, 0xa1, v200
	v_mov_b32_e32 v1, v201
	v_lshlrev_b64 v[0:1], 14, v[0:1]
	v_lshl_add_u64 v[0:1], v[6:7], 0, v[0:1]
	global_load_dwordx4 v[16:19], v[0:1], off offset:16
	global_load_dwordx4 v[20:23], v[0:1], off
	v_or_b32_e32 v0, 0xa2, v200
	v_mov_b32_e32 v1, v201
	v_lshlrev_b64 v[0:1], 14, v[0:1]
	v_lshl_add_u64 v[0:1], v[6:7], 0, v[0:1]
	global_load_dwordx4 v[24:27], v[0:1], off offset:16
	global_load_dwordx4 v[28:31], v[0:1], off
	v_or_b32_e32 v0, 0xa3, v200
	v_mov_b32_e32 v1, v201
	v_lshlrev_b64 v[0:1], 14, v[0:1]
	v_lshl_add_u64 v[0:1], v[6:7], 0, v[0:1]
	global_load_dwordx4 v[32:35], v[0:1], off offset:16
	global_load_dwordx4 v[36:39], v[0:1], off
	v_or_b32_e32 v0, 0xa4, v200
	v_mov_b32_e32 v1, v201
	v_lshlrev_b64 v[0:1], 14, v[0:1]
	v_lshl_add_u64 v[0:1], v[6:7], 0, v[0:1]
	global_load_dwordx4 v[40:43], v[0:1], off offset:16
	global_load_dwordx4 v[44:47], v[0:1], off
	v_or_b32_e32 v0, 0xa5, v200
	v_mov_b32_e32 v1, v201
	v_lshlrev_b64 v[0:1], 14, v[0:1]
	v_lshl_add_u64 v[0:1], v[6:7], 0, v[0:1]
	global_load_dwordx4 v[48:51], v[0:1], off offset:16
	global_load_dwordx4 v[52:55], v[0:1], off
	v_or_b32_e32 v0, 0xa6, v200
	v_mov_b32_e32 v1, v201
	v_lshlrev_b64 v[0:1], 14, v[0:1]
	v_lshl_add_u64 v[0:1], v[6:7], 0, v[0:1]
	v_cvt_pk_f16_f32 v117, v60, v68
	v_cvt_pk_f16_f32 v240, v61, v69
	v_cvt_pk_f16_f32 v232, v62, v70
	global_load_dwordx4 v[56:59], v[0:1], off offset:16
	global_load_dwordx4 v[60:63], v[0:1], off
	v_or_b32_e32 v0, 0xa7, v200
	v_mov_b32_e32 v1, v201
	v_lshlrev_b64 v[0:1], 14, v[0:1]
	v_lshl_add_u64 v[0:1], v[6:7], 0, v[0:1]
	global_load_dwordx4 v[64:67], v[0:1], off offset:16
	global_load_dwordx4 v[68:71], v[0:1], off
	v_or_b32_e32 v0, 0xc0, v200
	v_mov_b32_e32 v1, v201
	v_lshlrev_b64 v[0:1], 14, v[0:1]
	v_lshl_add_u64 v[0:1], v[6:7], 0, v[0:1]
	v_accvgpr_write_b32 a19, v117
	v_accvgpr_write_b32 a51, v240
	v_accvgpr_write_b32 a83, v232
	s_waitcnt vmcnt(13)
	v_cvt_pk_f16_f32 v255, v8, v16
	s_waitcnt vmcnt(12)
	v_cvt_pk_f16_f32 v110, v12, v20
	v_cvt_pk_f16_f32 v204, v13, v21
	v_cvt_pk_f16_f32 v251, v9, v17
	v_cvt_pk_f16_f32 v196, v14, v22
	v_cvt_pk_f16_f32 v247, v10, v18
	v_cvt_pk_f16_f32 v212, v15, v23
	v_cvt_pk_f16_f32 v239, v11, v19
	global_load_dwordx4 v[8:11], v[0:1], off offset:16
	global_load_dwordx4 v[12:15], v[0:1], off
	v_or_b32_e32 v0, 0xc1, v200
	v_mov_b32_e32 v1, v201
	v_lshlrev_b64 v[0:1], 14, v[0:1]
	v_lshl_add_u64 v[0:1], v[6:7], 0, v[0:1]
	global_load_dwordx4 v[16:19], v[0:1], off offset:16
	global_load_dwordx4 v[20:23], v[0:1], off
	v_or_b32_e32 v0, 0xc2, v200
	v_mov_b32_e32 v1, v201
	v_lshlrev_b64 v[0:1], 14, v[0:1]
	v_lshl_add_u64 v[0:1], v[6:7], 0, v[0:1]
	s_waitcnt vmcnt(12)
	v_cvt_pk_f16_f32 v111, v28, v36
	v_cvt_pk_f16_f32 v254, v24, v32
	v_cvt_pk_f16_f32 v180, v29, v37
	v_cvt_pk_f16_f32 v250, v25, v33
	v_cvt_pk_f16_f32 v213, v30, v38
	v_cvt_pk_f16_f32 v246, v26, v34
	v_cvt_pk_f16_f32 v216, v31, v39
	v_cvt_pk_f16_f32 v238, v27, v35
	global_load_dwordx4 v[24:27], v[0:1], off offset:16
	global_load_dwordx4 v[28:31], v[0:1], off
	v_or_b32_e32 v0, 0xc3, v200
	v_mov_b32_e32 v1, v201
	v_lshlrev_b64 v[0:1], 14, v[0:1]
	v_lshl_add_u64 v[0:1], v[6:7], 0, v[0:1]
	global_load_dwordx4 v[32:35], v[0:1], off offset:16
	global_load_dwordx4 v[36:39], v[0:1], off
	v_or_b32_e32 v0, 0xc4, v200
	v_mov_b32_e32 v1, v201
	v_lshlrev_b64 v[0:1], 14, v[0:1]
	v_lshl_add_u64 v[0:1], v[6:7], 0, v[0:1]
	s_waitcnt vmcnt(12)
	v_cvt_pk_f16_f32 v112, v44, v52
	v_cvt_pk_f16_f32 v253, v40, v48
	v_cvt_pk_f16_f32 v181, v45, v53
	v_cvt_pk_f16_f32 v249, v41, v49
	v_cvt_pk_f16_f32 v219, v46, v54
	v_cvt_pk_f16_f32 v244, v42, v50
	v_cvt_pk_f16_f32 v218, v47, v55
	v_cvt_pk_f16_f32 v237, v43, v51
	global_load_dwordx4 v[40:43], v[0:1], off offset:16
	global_load_dwordx4 v[44:47], v[0:1], off
	v_or_b32_e32 v0, 0xc5, v200
	v_mov_b32_e32 v1, v201
	v_lshlrev_b64 v[0:1], 14, v[0:1]
	v_lshl_add_u64 v[0:1], v[6:7], 0, v[0:1]
	global_load_dwordx4 v[48:51], v[0:1], off offset:16
	global_load_dwordx4 v[52:55], v[0:1], off
	v_or_b32_e32 v0, 0xc6, v200
	v_mov_b32_e32 v1, v201
	v_lshlrev_b64 v[0:1], 14, v[0:1]
	v_lshl_add_u64 v[0:1], v[6:7], 0, v[0:1]
	s_waitcnt vmcnt(12)
	v_cvt_pk_f16_f32 v113, v60, v68
	v_cvt_pk_f16_f32 v252, v56, v64
	v_cvt_pk_f16_f32 v183, v61, v69
	v_cvt_pk_f16_f32 v248, v57, v65
	v_cvt_pk_f16_f32 v222, v62, v70
	v_cvt_pk_f16_f32 v242, v58, v66
	v_cvt_pk_f16_f32 v221, v63, v71
	v_cvt_pk_f16_f32 v236, v59, v67
	global_load_dwordx4 v[56:59], v[0:1], off offset:16
	global_load_dwordx4 v[60:63], v[0:1], off
	v_or_b32_e32 v0, 0xc7, v200
	v_mov_b32_e32 v1, v201
	v_lshlrev_b64 v[0:1], 14, v[0:1]
	v_lshl_add_u64 v[0:1], v[6:7], 0, v[0:1]
	global_load_dwordx4 v[64:67], v[0:1], off offset:16
	global_load_dwordx4 v[68:71], v[0:1], off
	v_or_b32_e32 v0, 0xe0, v200
	v_mov_b32_e32 v1, v201
	v_lshlrev_b64 v[0:1], 14, v[0:1]
	v_lshl_add_u64 v[0:1], v[6:7], 0, v[0:1]
	v_accvgpr_write_b32 a20, v110
	v_accvgpr_write_b32 a21, v111
	v_accvgpr_write_b32 a22, v112
	v_accvgpr_write_b32 a23, v113
	v_accvgpr_write_b32 a52, v204
	v_accvgpr_write_b32 a53, v180
	v_accvgpr_write_b32 a54, v181
	v_accvgpr_write_b32 a55, v183
	v_accvgpr_write_b32 a84, v196
	v_accvgpr_write_b32 a85, v213
	v_accvgpr_write_b32 a86, v219
	v_accvgpr_write_b32 a87, v222
	v_accvgpr_write_b32 a116, v212
	v_accvgpr_write_b32 a117, v216
	v_accvgpr_write_b32 a118, v218
	v_accvgpr_write_b32 a119, v221
	v_accvgpr_write_b32 a148, v255
	v_accvgpr_write_b32 a149, v254
	v_accvgpr_write_b32 a150, v253
	v_accvgpr_write_b32 a151, v252
	s_waitcnt vmcnt(13)
	v_cvt_pk_f16_f32 v167, v8, v16
	s_waitcnt vmcnt(12)
	v_cvt_pk_f16_f32 v190, v12, v20
	v_cvt_pk_f16_f32 v146, v13, v21
	v_cvt_pk_f16_f32 v171, v9, v17
	v_cvt_pk_f16_f32 v159, v14, v22
	v_cvt_pk_f16_f32 v176, v10, v18
	v_cvt_pk_f16_f32 v163, v15, v23
	v_cvt_pk_f16_f32 v189, v11, v19
	global_load_dwordx4 v[8:11], v[0:1], off offset:16
	global_load_dwordx4 v[12:15], v[0:1], off
	v_or_b32_e32 v0, 0xe1, v200
	v_mov_b32_e32 v1, v201
	v_lshlrev_b64 v[0:1], 14, v[0:1]
	v_lshl_add_u64 v[0:1], v[6:7], 0, v[0:1]
	global_load_dwordx4 v[16:19], v[0:1], off offset:16
	global_load_dwordx4 v[20:23], v[0:1], off
	v_or_b32_e32 v0, 0xe2, v200
	v_mov_b32_e32 v1, v201
	v_lshlrev_b64 v[0:1], 14, v[0:1]
	v_lshl_add_u64 v[0:1], v[6:7], 0, v[0:1]
	s_waitcnt vmcnt(13)
	v_cvt_pk_f16_f32 v168, v24, v32
	s_waitcnt vmcnt(12)
	v_cvt_pk_f16_f32 v224, v28, v36
	v_cvt_pk_f16_f32 v147, v29, v37
	v_cvt_pk_f16_f32 v172, v25, v33
	v_cvt_pk_f16_f32 v160, v30, v38
	v_cvt_pk_f16_f32 v177, v26, v34
	v_cvt_pk_f16_f32 v164, v31, v39
	v_cvt_pk_f16_f32 v191, v27, v35
	global_load_dwordx4 v[24:27], v[0:1], off offset:16
	global_load_dwordx4 v[28:31], v[0:1], off
	v_or_b32_e32 v0, 0xe3, v200
	v_mov_b32_e32 v1, v201
	v_lshlrev_b64 v[0:1], 14, v[0:1]
	v_lshl_add_u64 v[0:1], v[6:7], 0, v[0:1]
	global_load_dwordx4 v[32:35], v[0:1], off offset:16
	global_load_dwordx4 v[36:39], v[0:1], off
	v_or_b32_e32 v0, 0xe4, v200
	v_mov_b32_e32 v1, v201
	v_lshlrev_b64 v[0:1], 14, v[0:1]
	v_lshl_add_u64 v[0:1], v[6:7], 0, v[0:1]
	s_waitcnt vmcnt(13)
	v_cvt_pk_f16_f32 v169, v40, v48
	s_waitcnt vmcnt(12)
	v_cvt_pk_f16_f32 v223, v44, v52
	v_cvt_pk_f16_f32 v148, v45, v53
	v_cvt_pk_f16_f32 v174, v41, v49
	v_cvt_pk_f16_f32 v161, v46, v54
	v_cvt_pk_f16_f32 v178, v42, v50
	v_cvt_pk_f16_f32 v165, v47, v55
	v_cvt_pk_f16_f32 v192, v43, v51
	global_load_dwordx4 v[40:43], v[0:1], off offset:16
	global_load_dwordx4 v[44:47], v[0:1], off
	v_or_b32_e32 v0, 0xe5, v200
	v_mov_b32_e32 v1, v201
	v_lshlrev_b64 v[0:1], 14, v[0:1]
	v_lshl_add_u64 v[0:1], v[6:7], 0, v[0:1]
	global_load_dwordx4 v[48:51], v[0:1], off offset:16
	global_load_dwordx4 v[52:55], v[0:1], off
	v_or_b32_e32 v0, 0xe6, v200
	v_mov_b32_e32 v1, v201
	v_lshlrev_b64 v[0:1], 14, v[0:1]
	v_lshl_add_u64 v[0:1], v[6:7], 0, v[0:1]
	v_or_b32_e32 v200, 0xe7, v200
	s_waitcnt vmcnt(12)
	v_cvt_pk_f16_f32 v194, v60, v68
	v_cvt_pk_f16_f32 v170, v56, v64
	v_cvt_pk_f16_f32 v149, v61, v69
	v_cvt_pk_f16_f32 v175, v57, v65
	v_cvt_pk_f16_f32 v162, v62, v70
	v_cvt_pk_f16_f32 v179, v58, v66
	v_cvt_pk_f16_f32 v166, v63, v71
	v_cvt_pk_f16_f32 v195, v59, v67
	global_load_dwordx4 v[56:59], v[0:1], off offset:16
	global_load_dwordx4 v[60:63], v[0:1], off
	v_lshlrev_b64 v[0:1], 14, v[200:201]
	v_lshl_add_u64 v[0:1], v[6:7], 0, v[0:1]
	global_load_dwordx4 v[64:67], v[0:1], off offset:16
	global_load_dwordx4 v[68:71], v[0:1], off
	v_or_b32_e32 v200, s14, v217
	v_lshlrev_b64 v[0:1], 14, v[200:201]
	v_accvgpr_write_b32 a24, v190
	v_accvgpr_write_b32 a25, v224
	v_accvgpr_write_b32 a26, v223
	v_accvgpr_write_b32 a27, v194
	v_accvgpr_write_b32 a56, v146
	v_accvgpr_write_b32 a57, v147
	v_accvgpr_write_b32 a58, v148
	v_accvgpr_write_b32 a59, v149
	v_accvgpr_write_b32 a88, v159
	v_accvgpr_write_b32 a89, v160
	v_accvgpr_write_b32 a90, v161
	v_accvgpr_write_b32 a91, v162
	v_accvgpr_write_b32 a120, v163
	v_accvgpr_write_b32 a121, v164
	v_accvgpr_write_b32 a122, v165
	v_accvgpr_write_b32 a123, v166
	v_accvgpr_write_b32 a152, v167
	v_accvgpr_write_b32 a153, v168
	v_accvgpr_write_b32 a154, v169
	v_accvgpr_write_b32 a155, v170
	v_accvgpr_write_b32 a180, v251
	v_accvgpr_write_b32 a181, v250
	v_accvgpr_write_b32 a182, v249
	s_waitcnt vmcnt(13)
	v_cvt_pk_f16_f32 v134, v8, v16
	v_cvt_pk_f16_f32 v138, v9, v17
	v_cvt_pk_f16_f32 v142, v10, v18
	v_cvt_pk_f16_f32 v151, v11, v19
	s_waitcnt vmcnt(12)
	v_cvt_pk_f16_f32 v173, v12, v20
	v_cvt_pk_f16_f32 v118, v13, v21
	v_cvt_pk_f16_f32 v126, v14, v22
	v_cvt_pk_f16_f32 v130, v15, v23
	v_accvgpr_write_b32 a28, v173
	v_accvgpr_write_b32 a60, v118
	v_accvgpr_write_b32 a92, v126
	v_accvgpr_write_b32 a124, v130
	v_accvgpr_write_b32 a156, v134
	v_accvgpr_write_b32 a183, v248
	v_accvgpr_write_b32 a184, v171
	v_accvgpr_write_b32 a185, v172
	v_accvgpr_write_b32 a186, v174
	v_accvgpr_write_b32 a187, v175
	s_waitcnt vmcnt(9)
	v_cvt_pk_f16_f32 v135, v24, v32
	v_cvt_pk_f16_f32 v139, v25, v33
	v_cvt_pk_f16_f32 v143, v26, v34
	v_cvt_pk_f16_f32 v152, v27, v35
	s_waitcnt vmcnt(8)
	v_cvt_pk_f16_f32 v182, v28, v36
	v_cvt_pk_f16_f32 v119, v29, v37
	v_cvt_pk_f16_f32 v127, v30, v38
	v_cvt_pk_f16_f32 v131, v31, v39
	v_accvgpr_write_b32 a29, v182
	v_accvgpr_write_b32 a61, v119
	v_accvgpr_write_b32 a93, v127
	v_accvgpr_write_b32 a125, v131
	v_accvgpr_write_b32 a157, v135
	v_accvgpr_write_b32 a188, v138
	v_accvgpr_write_b32 a189, v139
	v_accvgpr_write_b32 a212, v247
	v_accvgpr_write_b32 a213, v246
	v_accvgpr_write_b32 a214, v244
	s_waitcnt vmcnt(5)
	v_cvt_pk_f16_f32 v136, v40, v48
	v_cvt_pk_f16_f32 v140, v41, v49
	v_cvt_pk_f16_f32 v144, v42, v50
	v_cvt_pk_f16_f32 v153, v43, v51
	s_waitcnt vmcnt(4)
	v_cvt_pk_f16_f32 v184, v44, v52
	v_cvt_pk_f16_f32 v120, v45, v53
	v_cvt_pk_f16_f32 v128, v46, v54
	v_cvt_pk_f16_f32 v132, v47, v55
	v_accvgpr_write_b32 a30, v184
	v_accvgpr_write_b32 a62, v120
	v_accvgpr_write_b32 a94, v128
	v_accvgpr_write_b32 a126, v132
	v_accvgpr_write_b32 a158, v136
	v_accvgpr_write_b32 a190, v140
	v_accvgpr_write_b32 a215, v242
	v_accvgpr_write_b32 a216, v176
	v_accvgpr_write_b32 a217, v177
	s_waitcnt vmcnt(1)
	v_cvt_pk_f16_f32 v137, v56, v64
	v_cvt_pk_f16_f32 v141, v57, v65
	v_lshl_add_u64 v[64:65], s[12:13], 0, v[4:5]
	v_lshl_add_u64 v[0:1], v[64:65], 0, v[0:1]
	global_load_dwordx4 v[4:7], v[0:1], off offset:16
	global_load_dwordx4 v[8:11], v[0:1], off
	v_or_b32_e32 v0, 1, v200
	v_mov_b32_e32 v1, v201
	v_lshlrev_b64 v[0:1], 14, v[0:1]
	v_lshl_add_u64 v[0:1], v[64:65], 0, v[0:1]
	global_load_dwordx4 v[12:15], v[0:1], off offset:16
	global_load_dwordx4 v[16:19], v[0:1], off
	v_or_b32_e32 v0, 2, v200
	v_mov_b32_e32 v1, v201
	v_lshlrev_b64 v[0:1], 14, v[0:1]
	v_lshl_add_u64 v[0:1], v[64:65], 0, v[0:1]
	global_load_dwordx4 v[20:23], v[0:1], off offset:16
	global_load_dwordx4 v[24:27], v[0:1], off
	v_or_b32_e32 v0, 3, v200
	v_mov_b32_e32 v1, v201
	v_lshlrev_b64 v[0:1], 14, v[0:1]
	v_lshl_add_u64 v[0:1], v[64:65], 0, v[0:1]
	global_load_dwordx4 v[28:31], v[0:1], off offset:16
	global_load_dwordx4 v[32:35], v[0:1], off
	v_or_b32_e32 v0, 4, v200
	v_mov_b32_e32 v1, v201
	v_lshlrev_b64 v[0:1], 14, v[0:1]
	v_lshl_add_u64 v[0:1], v[64:65], 0, v[0:1]
	global_load_dwordx4 v[36:39], v[0:1], off offset:16
	global_load_dwordx4 v[40:43], v[0:1], off
	v_or_b32_e32 v0, 5, v200
	v_mov_b32_e32 v1, v201
	v_lshlrev_b64 v[0:1], 14, v[0:1]
	v_lshl_add_u64 v[0:1], v[64:65], 0, v[0:1]
	global_load_dwordx4 v[44:47], v[0:1], off offset:16
	global_load_dwordx4 v[48:51], v[0:1], off
	v_or_b32_e32 v0, 6, v200
	v_mov_b32_e32 v1, v201
	v_lshlrev_b64 v[0:1], 14, v[0:1]
	v_lshl_add_u64 v[0:1], v[64:65], 0, v[0:1]
	v_cvt_pk_f16_f32 v145, v58, v66
	v_cvt_pk_f16_f32 v154, v59, v67
	global_load_dwordx4 v[52:55], v[0:1], off offset:16
	global_load_dwordx4 v[56:59], v[0:1], off
	v_or_b32_e32 v0, 7, v200
	v_mov_b32_e32 v1, v201
	v_lshlrev_b64 v[0:1], 14, v[0:1]
	v_lshl_add_u64 v[0:1], v[64:65], 0, v[0:1]
	s_waitcnt vmcnt(14)
	v_cvt_pk_f16_f32 v209, v60, v68
	v_cvt_pk_f16_f32 v121, v61, v69
	v_cvt_pk_f16_f32 v129, v62, v70
	v_cvt_pk_f16_f32 v133, v63, v71
	global_load_dwordx4 v[60:63], v[0:1], off offset:16
	global_load_dwordx4 v[66:69], v[0:1], off
	v_or_b32_e32 v0, 32, v200
	v_mov_b32_e32 v1, v201
	v_lshlrev_b64 v[0:1], 14, v[0:1]
	v_lshl_add_u64 v[0:1], v[64:65], 0, v[0:1]
	v_readfirstlane_b32 s12, v186
	s_lshl_b32 s13, s19, 3
	v_or_b32_e32 v214, s13, v150
	v_ashrrev_i32_e32 v215, 31, v214
	v_accvgpr_write_b32 a31, v209
	v_accvgpr_write_b32 a63, v121
	v_accvgpr_write_b32 a95, v129
	v_accvgpr_write_b32 a127, v133
	v_accvgpr_write_b32 a159, v137
	v_accvgpr_write_b32 a191, v141
	v_accvgpr_write_b32 a218, v178
	v_accvgpr_write_b32 a219, v179
	v_accvgpr_write_b32 a220, v142
	v_accvgpr_write_b32 a221, v143
	v_accvgpr_write_b32 a222, v144
	v_accvgpr_write_b32 a223, v145
	v_accvgpr_write_b32 a244, v239
	v_accvgpr_write_b32 a245, v238
	v_accvgpr_write_b32 a246, v237
	v_accvgpr_write_b32 a247, v236
	v_accvgpr_write_b32 a248, v189
	v_accvgpr_write_b32 a249, v191
	v_accvgpr_write_b32 a250, v192
	v_accvgpr_write_b32 a251, v195
	v_accvgpr_write_b32 a252, v151
	v_accvgpr_write_b32 a253, v152
	v_accvgpr_write_b32 a254, v153
	v_accvgpr_write_b32 a255, v154
	s_waitcnt vmcnt(13)
	v_cvt_pk_f16_f32 v74, v4, v12
	s_waitcnt vmcnt(12)
	v_cvt_pk_f16_f32 v70, v8, v16
	v_cvt_pk_f16_f32 v78, v9, v17
	v_cvt_pk_f16_f32 v82, v5, v13
	v_cvt_pk_f16_f32 v86, v10, v18
	v_cvt_pk_f16_f32 v2, v6, v14
	v_cvt_pk_f16_f32 v8, v7, v15
	s_waitcnt vmcnt(9)
	v_cvt_pk_f16_f32 v75, v20, v28
	s_waitcnt vmcnt(8)
	v_cvt_pk_f16_f32 v71, v24, v32
	v_cvt_pk_f16_f32 v79, v25, v33
	v_cvt_pk_f16_f32 v83, v21, v29
	v_cvt_pk_f16_f32 v87, v26, v34
	v_cvt_pk_f16_f32 v3, v22, v30
	v_cvt_pk_f16_f32 v27, v27, v35
	v_cvt_pk_f16_f32 v26, v11, v19
	v_cvt_pk_f16_f32 v9, v23, v31
	s_waitcnt vmcnt(5)
	v_cvt_pk_f16_f32 v76, v36, v44
	s_waitcnt vmcnt(4)
	v_cvt_pk_f16_f32 v72, v40, v48
	v_cvt_pk_f16_f32 v80, v41, v49
	v_cvt_pk_f16_f32 v84, v37, v45
	v_cvt_pk_f16_f32 v88, v42, v50
	v_cvt_pk_f16_f32 v4, v38, v46
	v_cvt_pk_f16_f32 v28, v43, v51
	v_cvt_pk_f16_f32 v10, v39, v47
	s_waitcnt vmcnt(1)
	v_cvt_pk_f16_f32 v77, v52, v60
	s_waitcnt vmcnt(0)
	v_cvt_pk_f16_f32 v73, v56, v66
	v_cvt_pk_f16_f32 v81, v57, v67
	v_cvt_pk_f16_f32 v85, v53, v61
	v_cvt_pk_f16_f32 v89, v58, v68
	v_cvt_pk_f16_f32 v5, v54, v62
	v_cvt_pk_f16_f32 v29, v59, v69
	v_cvt_pk_f16_f32 v11, v55, v63
	ds_write_b128 v95, v[70:73]
	ds_write_b128 v95, v[78:81] offset:1024
	ds_write_b128 v95, v[86:89] offset:2048
	ds_write_b128 v95, v[26:29] offset:3072
	ds_write_b128 v95, v[74:77] offset:4096
	ds_write_b128 v95, v[82:85] offset:5120
	ds_write_b128 v95, v[2:5] offset:6144
	ds_write_b128 v95, v[8:11] offset:7168
	global_load_dwordx4 v[4:7], v[0:1], off offset:16
	global_load_dwordx4 v[12:15], v[0:1], off
	v_or_b32_e32 v0, 33, v200
	v_mov_b32_e32 v1, v201
	v_lshlrev_b64 v[0:1], 14, v[0:1]
	v_lshl_add_u64 v[0:1], v[64:65], 0, v[0:1]
	global_load_dwordx4 v[8:11], v[0:1], off offset:16
	global_load_dwordx4 v[16:19], v[0:1], off
	v_or_b32_e32 v0, 34, v200
	v_mov_b32_e32 v1, v201
	v_lshlrev_b64 v[0:1], 14, v[0:1]
	v_lshl_add_u64 v[0:1], v[64:65], 0, v[0:1]
	global_load_dwordx4 v[20:23], v[0:1], off offset:16
	global_load_dwordx4 v[32:35], v[0:1], off
	v_or_b32_e32 v0, 35, v200
	v_mov_b32_e32 v1, v201
	v_lshlrev_b64 v[0:1], 14, v[0:1]
	v_lshl_add_u64 v[0:1], v[64:65], 0, v[0:1]
	global_load_dwordx4 v[24:27], v[0:1], off offset:16
	global_load_dwordx4 v[40:43], v[0:1], off
	v_or_b32_e32 v0, 36, v200
	v_mov_b32_e32 v1, v201
	v_lshlrev_b64 v[0:1], 14, v[0:1]
	v_lshl_add_u64 v[0:1], v[64:65], 0, v[0:1]
	global_load_dwordx4 v[28:31], v[0:1], off offset:16
	global_load_dwordx4 v[44:47], v[0:1], off
	v_or_b32_e32 v0, 37, v200
	v_mov_b32_e32 v1, v201
	v_lshlrev_b64 v[0:1], 14, v[0:1]
	v_lshl_add_u64 v[0:1], v[64:65], 0, v[0:1]
	global_load_dwordx4 v[36:39], v[0:1], off offset:16
	global_load_dwordx4 v[48:51], v[0:1], off
	v_or_b32_e32 v0, 38, v200
	v_mov_b32_e32 v1, v201
	v_lshlrev_b64 v[0:1], 14, v[0:1]
	v_lshl_add_u64 v[0:1], v[64:65], 0, v[0:1]
	global_load_dwordx4 v[52:55], v[0:1], off offset:16
	global_load_dwordx4 v[56:59], v[0:1], off
	v_or_b32_e32 v0, 39, v200
	v_mov_b32_e32 v1, v201
	v_lshlrev_b64 v[0:1], 14, v[0:1]
	v_lshl_add_u64 v[0:1], v[64:65], 0, v[0:1]
	global_load_dwordx4 v[60:63], v[0:1], off offset:16
	global_load_dwordx4 v[66:69], v[0:1], off
	v_or_b32_e32 v0, s0, v193
	v_lshlrev_b32_e32 v94, 4, v0
	v_or_b32_e32 v0, 0x3c00, v94
	v_mov_b32_e32 v1, v201
	v_bfe_u32 v193, v193, 3, 1
	v_cmp_gt_u32_e64 s[0:1], 8, v220
	s_waitcnt vmcnt(13)
	v_cvt_pk_f16_f32 v74, v4, v8
	s_waitcnt vmcnt(12)
	v_cvt_pk_f16_f32 v70, v12, v16
	v_cvt_pk_f16_f32 v78, v13, v17
	v_cvt_pk_f16_f32 v2, v14, v18
	v_cvt_pk_f16_f32 v12, v7, v11
	v_cvt_pk_f16_f32 v82, v5, v9
	v_cvt_pk_f16_f32 v86, v6, v10
	s_waitcnt vmcnt(9)
	v_cvt_pk_f16_f32 v13, v23, v27
	s_waitcnt vmcnt(8)
	v_cvt_pk_f16_f32 v71, v32, v40
	v_cvt_pk_f16_f32 v3, v34, v42
	v_cvt_pk_f16_f32 v34, v15, v19
	v_cvt_pk_f16_f32 v75, v20, v24
	v_cvt_pk_f16_f32 v79, v33, v41
	v_cvt_pk_f16_f32 v83, v21, v25
	v_cvt_pk_f16_f32 v87, v22, v26
	v_cvt_pk_f16_f32 v35, v35, v43
	s_waitcnt vmcnt(5)
	v_cvt_pk_f16_f32 v14, v31, v39
	s_waitcnt vmcnt(4)
	v_cvt_pk_f16_f32 v72, v44, v48
	v_cvt_pk_f16_f32 v76, v28, v36
	v_cvt_pk_f16_f32 v80, v45, v49
	v_cvt_pk_f16_f32 v84, v29, v37
	v_cvt_pk_f16_f32 v4, v46, v50
	v_cvt_pk_f16_f32 v88, v30, v38
	v_cvt_pk_f16_f32 v36, v47, v51
	s_waitcnt vmcnt(1)
	v_cvt_pk_f16_f32 v15, v55, v63
	s_waitcnt vmcnt(0)
	v_cvt_pk_f16_f32 v73, v56, v66
	v_cvt_pk_f16_f32 v77, v52, v60
	v_cvt_pk_f16_f32 v81, v57, v67
	v_cvt_pk_f16_f32 v85, v53, v61
	v_cvt_pk_f16_f32 v5, v58, v68
	v_cvt_pk_f16_f32 v89, v54, v62
	v_cvt_pk_f16_f32 v37, v59, v69
	ds_write_b128 v95, v[70:73] offset:8192
	ds_write_b128 v95, v[78:81] offset:9216
	ds_write_b128 v95, v[2:5] offset:10240
	ds_write_b128 v95, v[34:37] offset:11264
	ds_write_b128 v95, v[74:77] offset:12288
	ds_write_b128 v95, v[82:85] offset:13312
	ds_write_b128 v95, v[86:89] offset:14336
	ds_write_b128 v0, v[12:15]
	v_or_b32_e32 v0, 64, v200
	v_lshlrev_b64 v[0:1], 14, v[0:1]
	v_lshl_add_u64 v[0:1], v[64:65], 0, v[0:1]
	global_load_dwordx4 v[4:7], v[0:1], off offset:16
	global_load_dwordx4 v[8:11], v[0:1], off
	v_or_b32_e32 v0, 0x41, v200
	v_mov_b32_e32 v1, v201
	v_lshlrev_b64 v[0:1], 14, v[0:1]
	v_lshl_add_u64 v[0:1], v[64:65], 0, v[0:1]
	global_load_dwordx4 v[12:15], v[0:1], off offset:16
	global_load_dwordx4 v[16:19], v[0:1], off
	v_or_b32_e32 v0, 0x42, v200
	v_mov_b32_e32 v1, v201
	v_lshlrev_b64 v[0:1], 14, v[0:1]
	v_lshl_add_u64 v[0:1], v[64:65], 0, v[0:1]
	global_load_dwordx4 v[20:23], v[0:1], off offset:16
	global_load_dwordx4 v[28:31], v[0:1], off
	v_or_b32_e32 v0, 0x43, v200
	v_mov_b32_e32 v1, v201
	v_lshlrev_b64 v[0:1], 14, v[0:1]
	v_lshl_add_u64 v[0:1], v[64:65], 0, v[0:1]
	global_load_dwordx4 v[24:27], v[0:1], off offset:16
	global_load_dwordx4 v[32:35], v[0:1], off
	v_or_b32_e32 v0, 0x44, v200
	v_mov_b32_e32 v1, v201
	v_lshlrev_b64 v[0:1], 14, v[0:1]
	v_lshl_add_u64 v[0:1], v[64:65], 0, v[0:1]
	global_load_dwordx4 v[36:39], v[0:1], off offset:16
	global_load_dwordx4 v[40:43], v[0:1], off
	v_or_b32_e32 v0, 0x45, v200
	v_mov_b32_e32 v1, v201
	v_lshlrev_b64 v[0:1], 14, v[0:1]
	v_lshl_add_u64 v[0:1], v[64:65], 0, v[0:1]
	global_load_dwordx4 v[44:47], v[0:1], off offset:16
	global_load_dwordx4 v[48:51], v[0:1], off
	v_or_b32_e32 v0, 0x46, v200
	v_mov_b32_e32 v1, v201
	v_lshlrev_b64 v[0:1], 14, v[0:1]
	v_lshl_add_u64 v[0:1], v[64:65], 0, v[0:1]
	global_load_dwordx4 v[52:55], v[0:1], off offset:16
	global_load_dwordx4 v[56:59], v[0:1], off
	v_or_b32_e32 v0, 0x47, v200
	v_mov_b32_e32 v1, v201
	v_lshlrev_b64 v[0:1], 14, v[0:1]
	v_lshl_add_u64 v[0:1], v[64:65], 0, v[0:1]
	global_load_dwordx4 v[60:63], v[0:1], off offset:16
	global_load_dwordx4 v[66:69], v[0:1], off
	v_or_b32_e32 v0, 0x60, v200
	v_mov_b32_e32 v1, v201
	v_lshlrev_b64 v[0:1], 14, v[0:1]
	v_lshl_add_u64 v[0:1], v[64:65], 0, v[0:1]
	s_waitcnt vmcnt(13)
	v_cvt_pk_f16_f32 v74, v4, v12
	s_waitcnt vmcnt(12)
	v_cvt_pk_f16_f32 v70, v8, v16
	v_cvt_pk_f16_f32 v78, v9, v17
	v_cvt_pk_f16_f32 v82, v5, v13
	v_cvt_pk_f16_f32 v2, v10, v18
	v_cvt_pk_f16_f32 v86, v6, v14
	v_cvt_pk_f16_f32 v8, v7, v15
	s_waitcnt vmcnt(9)
	v_cvt_pk_f16_f32 v75, v20, v24
	s_waitcnt vmcnt(8)
	v_cvt_pk_f16_f32 v71, v28, v32
	v_cvt_pk_f16_f32 v79, v29, v33
	v_cvt_pk_f16_f32 v83, v21, v25
	v_cvt_pk_f16_f32 v3, v30, v34
	v_cvt_pk_f16_f32 v87, v22, v26
	v_cvt_pk_f16_f32 v31, v31, v35
	v_cvt_pk_f16_f32 v30, v11, v19
	v_cvt_pk_f16_f32 v9, v23, v27
	s_waitcnt vmcnt(5)
	v_cvt_pk_f16_f32 v76, v36, v44
	s_waitcnt vmcnt(4)
	v_cvt_pk_f16_f32 v72, v40, v48
	v_cvt_pk_f16_f32 v80, v41, v49
	v_cvt_pk_f16_f32 v84, v37, v45
	v_cvt_pk_f16_f32 v4, v42, v50
	v_cvt_pk_f16_f32 v88, v38, v46
	v_cvt_pk_f16_f32 v32, v43, v51
	v_cvt_pk_f16_f32 v10, v39, v47
	s_waitcnt vmcnt(1)
	v_cvt_pk_f16_f32 v77, v52, v60
	s_waitcnt vmcnt(0)
	v_cvt_pk_f16_f32 v73, v56, v66
	v_cvt_pk_f16_f32 v81, v57, v67
	v_cvt_pk_f16_f32 v85, v53, v61
	v_cvt_pk_f16_f32 v5, v58, v68
	v_cvt_pk_f16_f32 v89, v54, v62
	v_cvt_pk_f16_f32 v33, v59, v69
	v_cvt_pk_f16_f32 v11, v55, v63
	ds_write_b128 v95, v[70:73] offset:16384
	ds_write_b128 v95, v[78:81] offset:17408
	ds_write_b128 v95, v[2:5] offset:18432
	ds_write_b128 v95, v[30:33] offset:19456
	ds_write_b128 v95, v[74:77] offset:20480
	ds_write_b128 v95, v[82:85] offset:21504
	ds_write_b128 v95, v[86:89] offset:22528
	ds_write_b128 v95, v[8:11] offset:23552
	global_load_dwordx4 v[8:11], v[0:1], off offset:16
	global_load_dwordx4 v[40:43], v[0:1], off
	v_or_b32_e32 v0, 0x61, v200
	v_mov_b32_e32 v1, v201
	v_lshlrev_b64 v[0:1], 14, v[0:1]
	v_lshl_add_u64 v[0:1], v[64:65], 0, v[0:1]
	global_load_dwordx4 v[16:19], v[0:1], off offset:16
	global_load_dwordx4 v[48:51], v[0:1], off
	v_or_b32_e32 v0, 0x62, v200
	v_mov_b32_e32 v1, v201
	v_lshlrev_b64 v[0:1], 14, v[0:1]
	v_lshl_add_u64 v[0:1], v[64:65], 0, v[0:1]
	global_load_dwordx4 v[30:33], v[0:1], off offset:16
	global_load_dwordx4 v[56:59], v[0:1], off
	v_or_b32_e32 v0, 0x63, v200
	v_mov_b32_e32 v1, v201
	v_lshlrev_b64 v[0:1], 14, v[0:1]
	v_lshl_add_u64 v[0:1], v[64:65], 0, v[0:1]
	global_load_dwordx4 v[34:37], v[0:1], off offset:16
	global_load_dwordx4 v[60:63], v[0:1], off
	v_or_b32_e32 v0, 0x64, v200
	v_mov_b32_e32 v1, v201
	v_lshlrev_b64 v[0:1], 14, v[0:1]
	v_lshl_add_u64 v[0:1], v[64:65], 0, v[0:1]
	global_load_dwordx4 v[44:47], v[0:1], off offset:16
	global_load_dwordx4 v[72:75], v[0:1], off
	v_or_b32_e32 v0, 0x65, v200
	v_mov_b32_e32 v1, v201
	v_lshlrev_b64 v[0:1], 14, v[0:1]
	v_lshl_add_u64 v[0:1], v[64:65], 0, v[0:1]
	global_load_dwordx4 v[52:55], v[0:1], off offset:16
	global_load_dwordx4 v[80:83], v[0:1], off
	v_or_b32_e32 v0, 0x66, v200
	v_mov_b32_e32 v1, v201
	v_lshlrev_b64 v[0:1], 14, v[0:1]
	v_lshl_add_u64 v[0:1], v[64:65], 0, v[0:1]
	v_or_b32_e32 v200, 0x67, v200
	global_load_dwordx4 v[68:71], v[0:1], off offset:16
	global_load_dwordx4 v[84:87], v[0:1], off
	v_lshlrev_b64 v[0:1], 14, v[200:201]
	v_lshl_add_u64 v[0:1], v[64:65], 0, v[0:1]
	global_load_dwordx4 v[76:79], v[0:1], off offset:16
	s_nop 0
	global_load_dwordx4 v[0:3], v[0:1], off
	v_lshlrev_b32_e32 v200, 5, v109
	s_waitcnt vmcnt(13)
	v_cvt_pk_f16_f32 v4, v8, v16
	s_waitcnt vmcnt(12)
	v_cvt_pk_f16_f32 v64, v40, v48
	v_cvt_pk_f16_f32 v20, v41, v49
	v_cvt_pk_f16_f32 v12, v9, v17
	v_cvt_pk_f16_f32 v28, v42, v50
	v_cvt_pk_f16_f32 v24, v10, v18
	v_cvt_pk_f16_f32 v38, v43, v51
	s_waitcnt vmcnt(9)
	v_cvt_pk_f16_f32 v5, v30, v34
	s_waitcnt vmcnt(8)
	v_cvt_pk_f16_f32 v65, v56, v60
	v_cvt_pk_f16_f32 v13, v31, v35
	v_cvt_pk_f16_f32 v25, v32, v36
	v_cvt_pk_f16_f32 v33, v33, v37
	v_cvt_pk_f16_f32 v32, v11, v19
	v_cvt_pk_f16_f32 v21, v57, v61
	v_cvt_pk_f16_f32 v29, v58, v62
	v_cvt_pk_f16_f32 v39, v59, v63
	s_waitcnt vmcnt(5)
	v_cvt_pk_f16_f32 v26, v46, v54
	v_add_u32_e32 v54, s2, v208
	s_waitcnt vmcnt(4)
	v_cvt_pk_f16_f32 v66, v72, v80
	v_cvt_pk_f16_f32 v34, v47, v55
	v_ashrrev_i32_e32 v55, 31, v54
	v_cvt_pk_f16_f32 v6, v44, v52
	v_cvt_pk_f16_f32 v22, v73, v81
	v_cvt_pk_f16_f32 v14, v45, v53
	v_cvt_pk_f16_f32 v30, v74, v82
	s_waitcnt vmcnt(1)
	v_cvt_pk_f16_f32 v35, v71, v79
	s_waitcnt vmcnt(0)
	v_cvt_pk_f16_f32 v67, v84, v0
	v_or_b32_e32 v0, 0x7c00, v94
	v_cvt_pk_f16_f32 v7, v68, v76
	v_cvt_pk_f16_f32 v23, v85, v1
	v_cvt_pk_f16_f32 v15, v69, v77
	v_cvt_pk_f16_f32 v31, v86, v2
	v_cvt_pk_f16_f32 v27, v70, v78
	v_cvt_pk_f16_f32 v41, v87, v3
	v_cvt_pk_f16_f32 v40, v75, v83
	ds_write_b128 v95, v[64:67] offset:24576
	ds_write_b128 v95, v[20:23] offset:25600
	ds_write_b128 v95, v[28:31] offset:26624
	ds_write_b128 v95, v[38:41] offset:27648
	ds_write_b128 v95, v[4:7] offset:28672
	ds_write_b128 v95, v[12:15] offset:29696
	ds_write_b128 v95, v[24:27] offset:30720
	ds_write_b128 v0, v[32:35]
	v_lshl_add_u64 v[0:1], v[54:55], 2, s[4:5]
	global_load_dword v185, v[0:1], off
	v_add_u32_e32 v0, 0x400, v54
	v_ashrrev_i32_e32 v1, 31, v0
	v_lshl_add_u64 v[0:1], v[0:1], 2, s[4:5]
	global_load_dword v186, v[0:1], off
	v_add_u32_e32 v0, 0x800, v54
	v_ashrrev_i32_e32 v1, 31, v0
	v_lshl_add_u64 v[0:1], v[0:1], 2, s[4:5]
	global_load_dword v187, v[0:1], off
	v_add_u32_e32 v0, 0xc00, v54
	v_ashrrev_i32_e32 v1, 31, v0
	v_lshl_add_u64 v[0:1], v[0:1], 2, s[4:5]
	global_load_dword v188, v[0:1], off
	v_lshlrev_b64 v[0:1], 20, v[214:215]
	v_lshl_add_u64 v[0:1], s[16:17], 0, v[0:1]
	v_lshl_add_u64 v[0:1], s[14:15], 2, v[0:1]
	v_lshl_add_u64 v[210:211], v[0:1], 0, v[200:201]
	global_load_dwordx4 v[4:7], v[210:211], off offset:256
	global_load_dwordx4 v[8:11], v[210:211], off offset:272
	global_load_dwordx4 v[14:17], v[210:211], off offset:384
	global_load_dwordx4 v[18:21], v[210:211], off offset:400
	v_lshlrev_b32_e32 v0, 4, v198
	s_waitcnt lgkmcnt(0)
	s_barrier
	ds_read_b128 v[96:99], v0 offset:23552
	ds_read_b128 v[92:95], v0 offset:22528
	ds_read_b128 v[88:91], v0 offset:21504
	ds_read_b128 v[60:63], v0 offset:20480
	ds_read_b128 v[64:67], v0 offset:19456
	ds_read_b128 v[68:71], v0 offset:18432
	ds_read_b128 v[72:75], v0 offset:17408
	ds_read_b128 v[76:79], v0 offset:16384
	v_mov_b64_e32 v[44:45], s[26:27]
	v_mov_b64_e32 v[40:41], s[26:27]
	v_mov_b64_e32 v[22:23], s[24:25]
	v_mov_b64_e32 v[28:29], s[26:27]
	v_mov_b64_e32 v[32:33], s[26:27]
	v_mov_b64_e32 v[36:37], s[26:27]
	v_mov_b64_e32 v[42:43], s[24:25]
	v_mov_b64_e32 v[38:39], s[24:25]
	v_mov_b64_e32 v[24:25], s[26:27]
	v_mov_b64_e32 v[26:27], s[24:25]
	v_mov_b64_e32 v[30:31], s[24:25]
	v_mov_b64_e32 v[34:35], s[24:25]
	s_or_b32 s4, s3, s13
	s_ashr_i32 s5, s4, 31
	s_lshl_b64 s[4:5], s[4:5], 20
	s_add_u32 s4, s16, s4
	s_addc_u32 s5, s17, s5
	s_cmp_lg_u32 s12, 0
	v_mov_b32_e32 v200, v201
	s_waitcnt vmcnt(3)
	v_cvt_pk_f16_f32 v101, v6, v7
	s_waitcnt vmcnt(2)
	v_cvt_pk_f16_f32 v103, v10, v11
	v_cvt_pk_f16_f32 v102, v8, v9
	v_cvt_pk_f16_f32 v100, v4, v5
	ds_read_b128 v[80:83], v0 offset:31744
	ds_read_b128 v[84:87], v0 offset:30720
	ds_read_b128 v[56:59], v0 offset:29696
	ds_read_b128 v[50:53], v0 offset:28672
	ds_read_b128 v[46:49], v0 offset:27648
	ds_read_b128 v[8:11], v0 offset:26624
	ds_read_b128 v[4:7], v0 offset:25600
	ds_read_b128 v[0:3], v0 offset:24576
	s_waitcnt vmcnt(0)
	v_cvt_pk_f16_f32 v107, v20, v21
	v_cvt_pk_f16_f32 v106, v18, v19
	v_cvt_pk_f16_f32 v105, v16, v17
	v_cvt_pk_f16_f32 v104, v14, v15
	v_mov_b64_e32 v[14:15], s[24:25]
	v_mov_b64_e32 v[18:19], s[24:25]
	v_mov_b64_e32 v[16:17], s[26:27]
	v_mov_b64_e32 v[20:21], s[26:27]
	s_waitcnt lgkmcnt(8)
	s_nop 1
	v_mfma_f32_16x16x32_f16 v[42:45], v[76:79], v[100:103], v[42:45]
	v_mfma_f32_16x16x32_f16 v[38:41], v[72:75], v[100:103], v[38:41]
	v_mfma_f32_16x16x32_f16 v[14:17], v[68:71], v[100:103], v[14:17]
	v_mfma_f32_16x16x32_f16 v[18:21], v[64:67], v[100:103], v[18:21]
	v_mfma_f32_16x16x32_f16 v[22:25], v[60:63], v[100:103], v[22:25]
	v_mfma_f32_16x16x32_f16 v[26:29], v[88:91], v[100:103], v[26:29]
	v_mfma_f32_16x16x32_f16 v[30:33], v[92:95], v[100:103], v[30:33]
	v_mfma_f32_16x16x32_f16 v[34:37], v[96:99], v[100:103], v[34:37]
	v_lshlrev_b32_e32 v103, 4, v150
	s_waitcnt lgkmcnt(0)
	s_nop 1
	v_mfma_f32_16x16x32_f16 v[42:45], v[0:3], v[104:107], v[42:45]
	v_mfma_f32_16x16x32_f16 v[38:41], v[4:7], v[104:107], v[38:41]
	v_mfma_f32_16x16x32_f16 v[14:17], v[8:11], v[104:107], v[14:17]
	v_mfma_f32_16x16x32_f16 v[18:21], v[46:49], v[104:107], v[18:21]
	v_mfma_f32_16x16x32_f16 v[22:25], v[50:53], v[104:107], v[22:25]
	v_mfma_f32_16x16x32_f16 v[26:29], v[56:59], v[104:107], v[26:29]
	v_mfma_f32_16x16x32_f16 v[30:33], v[84:87], v[104:107], v[30:33]
	v_mfma_f32_16x16x32_f16 v[34:37], v[80:83], v[104:107], v[34:37]
	v_lshlrev_b32_e32 v0, 11, v193
	v_mov_b32_e32 v1, v201
	s_nop 15
	s_nop 7
	v_lshl_add_u64 v[0:1], v[210:211], 0, v[0:1]
	v_cndmask_b32_e64 v6, 0, v42, s[0:1]
	v_cndmask_b32_e64 v7, 0, v43, s[0:1]
	v_cndmask_b32_e64 v8, 0, v44, s[0:1]
	v_cndmask_b32_e64 v9, 0, v45, s[0:1]
	v_cndmask_b32_e64 v10, 0, v38, s[0:1]
	v_cndmask_b32_e64 v11, 0, v39, s[0:1]
	v_cndmask_b32_e64 v12, 0, v40, s[0:1]
	v_cndmask_b32_e64 v13, 0, v41, s[0:1]
	global_load_dwordx4 v[50:53], v[0:1], off offset:16
	global_load_dwordx4 v[46:49], v[0:1], off
	global_load_dwordx4 v[42:45], v[0:1], off offset:144
	global_load_dwordx4 v[38:41], v[0:1], off offset:128
	v_lshl_add_u32 v2, v220, 4, s14
	v_lshl_or_b32 v55, v207, 1, v2
	v_or_b32_e32 v2, s13, v220
	v_ashrrev_i32_e32 v3, 31, v2
	v_lshlrev_b32_e32 v0, 7, v109
	v_mov_b32_e32 v109, v201
	v_lshlrev_b64 v[2:3], 21, v[2:3]
	v_or3_b32 v104, v0, v103, s21
	v_lshl_add_u64 v[0:1], s[4:5], 0, v[108:109]
	s_cselect_b64 s[4:5], -1, 0
	v_lshl_add_u64 v[2:3], s[6:7], 0, v[2:3]
	s_ashr_i32 s3, s2, 31
	v_lshl_add_u64 v[2:3], s[2:3], 2, v[2:3]
	v_lshlrev_b32_e32 v4, 2, v208
	v_mov_b32_e32 v5, v201
	v_lshl_add_u64 v[96:97], v[2:3], 0, v[4:5]
	v_lshl_add_u32 v2, v214, 10, v54
	v_ashrrev_i32_e32 v3, 31, v2
	v_lshl_add_u64 v[2:3], v[2:3], 2, s[6:7]
	s_mov_b64 s[2:3], 0x8000000
	v_lshl_add_u64 v[98:99], v[2:3], 0, s[2:3]
	s_mov_b64 s[2:3], 0x8040000
	v_lshl_add_u64 v[100:101], v[2:3], 0, s[2:3]
	s_lshl_b32 s2, s19, 14
	s_lshl_b32 s3, s18, 9
	s_add_i32 s2, s2, s3
	v_mbcnt_lo_u32_b32 v2, -1, 0
	v_add_u32_e32 v106, s2, v55
	v_mbcnt_hi_u32_b32 v2, -1, v2
	v_mov_b64_e32 v[54:55], v[200:201]
	v_mov_b64_e32 v[58:59], v[200:201]
	v_cndmask_b32_e64 v14, 0, v14, s[0:1]
	v_cndmask_b32_e64 v15, 0, v15, s[0:1]
	v_cndmask_b32_e64 v16, 0, v16, s[0:1]
	v_cndmask_b32_e64 v17, 0, v17, s[0:1]
	v_cndmask_b32_e64 v18, 0, v18, s[0:1]
	v_cndmask_b32_e64 v19, 0, v19, s[0:1]
	v_cndmask_b32_e64 v20, 0, v20, s[0:1]
	v_cndmask_b32_e64 v21, 0, v21, s[0:1]
	v_cndmask_b32_e64 v22, 0, v22, s[0:1]
	v_cndmask_b32_e64 v23, 0, v23, s[0:1]
	v_cndmask_b32_e64 v24, 0, v24, s[0:1]
	v_cndmask_b32_e64 v25, 0, v25, s[0:1]
	v_cndmask_b32_e64 v26, 0, v26, s[0:1]
	v_cndmask_b32_e64 v27, 0, v27, s[0:1]
	v_cndmask_b32_e64 v28, 0, v28, s[0:1]
	v_cndmask_b32_e64 v29, 0, v29, s[0:1]
	v_cndmask_b32_e64 v30, 0, v30, s[0:1]
	v_cndmask_b32_e64 v31, 0, v31, s[0:1]
	v_cndmask_b32_e64 v32, 0, v32, s[0:1]
	v_cndmask_b32_e64 v33, 0, v33, s[0:1]
	v_cndmask_b32_e64 v34, 0, v34, s[0:1]
	v_cndmask_b32_e64 v35, 0, v35, s[0:1]
	v_cndmask_b32_e64 v36, 0, v36, s[0:1]
	v_cndmask_b32_e64 v37, 0, v37, s[0:1]
	v_lshlrev_b32_e32 v105, 9, v207
	s_mov_b64 s[6:7], 0
	s_mov_b32 s18, 0x40004000
	v_lshl_or_b32 v107, v2, 2, 32
	v_mov_b32_e32 v108, 0
	v_mov_b64_e32 v[56:57], v[202:203]
	v_mov_b64_e32 v[60:61], v[202:203]
	s_mov_b32 s24, 0
	v_lshl_add_u32 v166, s19, 14, v104
	v_mov_b32_e32 v177, 0
	s_not_b64 s[56:57], s[0:1]
	v_add_u32_e32 v79, 0x200, v166
	s_mov_b32 s37, 0x4038aa3b
	s_mov_b32 s38, 0xbfb8aa3b
	v_lshlrev_b32_e32 v222, 4, v198
	ds_read_b128 v[130:133], v222
	ds_read_b128 v[126:129], v222 offset:1024
	ds_read_b128 v[122:125], v222 offset:2048
	ds_read_b128 v[118:121], v222 offset:3072
	ds_read_b128 v[114:117], v222 offset:4096
	ds_read_b128 v[110:113], v222 offset:5120
	ds_read_b128 v[194:197], v222 offset:6144
	ds_read_b128 v[202:205], v222 offset:7168
	ds_read_b128 v[162:165], v222 offset:8192
	ds_read_b128 v[158:161], v222 offset:9216
	ds_read_b128 v[154:157], v222 offset:10240
	ds_read_b128 v[150:153], v222 offset:11264
	ds_read_b128 v[146:149], v222 offset:12288
	ds_read_b128 v[142:145], v222 offset:13312
	ds_read_b128 v[138:141], v222 offset:14336
	ds_read_b128 v[134:137], v222 offset:15360
	s_waitcnt vmcnt(0)
	v_mul_f32_e32 v185, 0xbfb8aa3b, v185
	v_mul_f32_e32 v186, 0xbfb8aa3b, v186
	v_mul_f32_e32 v187, 0x4038aa3b, v187
	v_mul_f32_e32 v188, 0xbfb8aa3b, v188
	v_cvt_pk_f16_f32 v180, v46, v47
	v_cvt_pk_f16_f32 v181, v48, v49
	v_cvt_pk_f16_f32 v182, v50, v51
	v_cvt_pk_f16_f32 v183, v52, v53
	v_cvt_pk_f16_f32 v218, v38, v39
	v_cvt_pk_f16_f32 v219, v40, v41
	v_cvt_pk_f16_f32 v220, v42, v43
	v_cvt_pk_f16_f32 v221, v44, v45
	s_mov_b32 s25, 1
	v_bitop3_b32 v2, s25, v193, 1 bitop3:0x6c
	v_add_u32_e32 v2, s25, v2
	v_min_i32_e32 v2, 0x1ff, v2
	s_and_b32 s12, s25, 1
	v_lshlrev_b32_e32 v200, 11, v2
	v_lshl_add_u64 v[2:3], v[210:211], 0, v[200:201]
	s_lshl_b32 s14, s12, 8
	v_lshl_add_u64 v[4:5], v[2:3], 0, s[14:15]
	global_load_dwordx4 v[46:49], v[4:5], off
	global_load_dwordx4 v[50:53], v[4:5], off offset:16
	global_load_dwordx4 v[38:41], v[4:5], off offset:128
	global_load_dwordx4 v[42:45], v[4:5], off offset:144
.Lstep_top:
	s_and_b32 s16, s24, 1
	s_cmp_eq_u32 s16, 0
	s_cselect_b64 s[2:3], s[0:1], s[56:57]
	v_cndmask_b32_e64 v78, v79, v166, s[2:3]
	s_xor_b32 s33, s16, 1
	s_lshl_b32 s28, s33, 17
	s_add_i32 s25, s24, 1
	s_add_i32 s27, s24, 2
	s_mov_b32 s17, 0
	s_cmp_eq_u32 s24, 0
	s_cbranch_scc1 .Lpoll_issued
	buffer_load_dwordx4 v[62:65], v78, s[8:11], s28 offen sc1
	buffer_load_dwordx4 v[66:69], v78, s[8:11], s28 offen offset:1024 sc1
	buffer_load_dwordx4 v[70:73], v78, s[8:11], s28 offen offset:2048 sc1
	buffer_load_dwordx4 v[74:77], v78, s[8:11], s28 offen offset:3072 sc1
.Lpoll_issued:
	s_waitcnt lgkmcnt(0)
	v_mfma_f32_16x16x32_f16 v[6:9], v[130:133], v[180:183], v[6:9]
	s_add_i32 s12, s24, -1
	s_bfe_i32 s13, s12, 0x10001
	v_mfma_f32_16x16x32_f16 v[10:13], v[126:129], v[180:183], v[10:13]
	s_and_b32 s30, s13, 0x40004000
	v_mov_b32_e32 v3, 0xbfffbfff
	v_mfma_f32_16x16x32_f16 v[14:17], v[122:125], v[180:183], v[14:17]
	v_cndmask_b32_e64 v167, 0, v3, s[2:3]
	s_lshl_b32 s34, s24, 13
	v_mfma_f32_16x16x32_f16 v[18:21], v[118:121], v[180:183], v[18:21]
	s_and_b32 s34, s34, 0x4000
	s_lshl_b32 s14, s24, 10
	v_mfma_f32_16x16x32_f16 v[22:25], v[114:117], v[180:183], v[22:25]
	v_lshl_add_u64 v[178:179], s[14:15], 2, v[96:97]
	v_bitop3_b32 v2, s27, v193, 1 bitop3:0x6c
	v_mfma_f32_16x16x32_f16 v[26:29], v[110:113], v[180:183], v[26:29]
	v_add_u32_e32 v2, s27, v2
	v_min_i32_e32 v2, 0x1ff, v2
	v_mfma_f32_16x16x32_f16 v[30:33], v[194:197], v[180:183], v[30:33]
	s_and_b32 s12, s27, 1
	v_lshlrev_b32_e32 v200, 11, v2
	v_mfma_f32_16x16x32_f16 v[34:37], v[202:205], v[180:183], v[34:37]
	v_lshl_add_u64 v[2:3], v[210:211], 0, v[200:201]
	s_lshl_b32 s14, s12, 8
	s_waitcnt lgkmcnt(0)
	v_mfma_f32_16x16x32_f16 v[6:9], v[162:165], v[218:221], v[6:9]
	v_lshl_add_u64 v[4:5], v[2:3], 0, s[14:15]
	s_lshl_b32 s35, s16, 14
	v_mfma_f32_16x16x32_f16 v[10:13], v[158:161], v[218:221], v[10:13]
	s_bitset1_b32 s35, 17
	s_add_i32 s26, s35, s21
	v_mfma_f32_16x16x32_f16 v[14:17], v[154:157], v[218:221], v[14:17]
	v_lshlrev_b32_e32 v2, 4, v217
	v_add3_u32 v174, s26, v2, v103
	v_mfma_f32_16x16x32_f16 v[18:21], v[150:153], v[218:221], v[18:21]
	s_lshl_b32 s12, s20, 4
	s_add_i32 s12, s12, s35
	v_mfma_f32_16x16x32_f16 v[22:25], v[146:149], v[218:221], v[22:25]
	v_add3_u32 v175, s12, v105, v103
	v_lshl_add_u32 v176, s16, 17, v106
	v_mfma_f32_16x16x32_f16 v[26:29], v[142:145], v[218:221], v[26:29]
	s_and_b32 s31, s24, 15
	s_and_b32 s12, s24, 0x1f0
	v_mfma_f32_16x16x32_f16 v[30:33], v[138:141], v[218:221], v[30:33]
	s_add_i32 s12, s23, s12
	s_min_i32 s12, s12, 0x1ff
	v_mfma_f32_16x16x32_f16 v[34:37], v[134:137], v[218:221], v[34:37]
	s_ashr_i32 s13, s12, 31
	s_lshl_b64 s[12:13], s[12:13], 11
	v_lshl_add_u64 v[172:173], v[0:1], 0, s[12:13]
	s_cmp_eq_u32 s24, 0
	s_cbranch_scc1 .Lfirst_step
	s_waitcnt vmcnt(3)
	v_bitop3_b32 v168, v62, v63, s30 bitop3:0x7e
	v_bitop3_b32 v169, v64, v65, s30 bitop3:0x7e
	v_bitop3_b32 v168, v168, v169, s18 bitop3:0xa8
	v_cmp_ne_u32_e32 vcc, 0, v168
	s_cbranch_vccnz .Lrestart0
	v_and_b32_e32 v224, v62, v167
	v_and_b32_e32 v225, v63, v167
	v_and_b32_e32 v226, v64, v167
	v_and_b32_e32 v227, v65, v167
	v_and_b32_dpp v228, v62, v167 row_ror:8 row_mask:0xf bank_mask:0xf
	v_and_b32_dpp v229, v63, v167 row_ror:8 row_mask:0xf bank_mask:0xf
	v_and_b32_dpp v230, v64, v167 row_ror:8 row_mask:0xf bank_mask:0xf
	v_and_b32_dpp v231, v65, v167 row_ror:8 row_mask:0xf bank_mask:0xf
	s_nop 1
.Lfast0:
	v_mfma_f32_16x16x32_f16 v[6:9], a[0:3], v[224:227], v[6:9]
	v_cvt_pk_f16_f32 v180, v46, v47
	v_cvt_pk_f16_f32 v181, v48, v49
	v_mfma_f32_16x16x32_f16 v[10:13], a[32:35], v[224:227], v[10:13]
	v_cvt_pk_f16_f32 v182, v50, v51
	v_cvt_pk_f16_f32 v183, v52, v53
	v_mfma_f32_16x16x32_f16 v[14:17], a[64:67], v[224:227], v[14:17]
	v_cvt_pk_f16_f32 v218, v38, v39
	v_cvt_pk_f16_f32 v219, v40, v41
	v_mfma_f32_16x16x32_f16 v[18:21], a[96:99], v[224:227], v[18:21]
	v_cvt_pk_f16_f32 v220, v42, v43
	v_cvt_pk_f16_f32 v221, v44, v45
	v_mfma_f32_16x16x32_f16 v[22:25], a[128:131], v[224:227], v[22:25]
	s_waitcnt vmcnt(2)
	v_mfma_f32_16x16x32_f16 v[26:29], a[160:163], v[224:227], v[26:29]
	v_bitop3_b32 v168, v66, v67, s30 bitop3:0x7e
	v_bitop3_b32 v169, v68, v69, s30 bitop3:0x7e
	v_mfma_f32_16x16x32_f16 v[30:33], a[192:195], v[224:227], v[30:33]
	v_bitop3_b32 v168, v168, v169, s18 bitop3:0xa8
	v_cmp_ne_u32_e32 vcc, 0, v168
	v_mfma_f32_16x16x32_f16 v[34:37], a[224:227], v[224:227], v[34:37]
	v_and_b32_e32 v232, v66, v167
	v_and_b32_e32 v233, v67, v167
	v_mfma_f32_16x16x32_f16 v[6:9], a[4:7], v[228:231], v[6:9]
	v_and_b32_e32 v234, v68, v167
	v_and_b32_e32 v235, v69, v167
	v_mfma_f32_16x16x32_f16 v[10:13], a[36:39], v[228:231], v[10:13]
	v_and_b32_dpp v236, v66, v167 row_ror:8 row_mask:0xf bank_mask:0xf
	v_and_b32_dpp v237, v67, v167 row_ror:8 row_mask:0xf bank_mask:0xf
	v_mfma_f32_16x16x32_f16 v[14:17], a[68:71], v[228:231], v[14:17]
	v_and_b32_dpp v238, v68, v167 row_ror:8 row_mask:0xf bank_mask:0xf
	v_and_b32_dpp v239, v69, v167 row_ror:8 row_mask:0xf bank_mask:0xf
	v_mfma_f32_16x16x32_f16 v[18:21], a[100:103], v[228:231], v[18:21]
	v_mfma_f32_16x16x32_f16 v[22:25], a[132:135], v[228:231], v[22:25]
	v_mfma_f32_16x16x32_f16 v[26:29], a[164:167], v[228:231], v[26:29]
	v_mfma_f32_16x16x32_f16 v[30:33], a[196:199], v[228:231], v[30:33]
	v_mfma_f32_16x16x32_f16 v[34:37], a[228:231], v[228:231], v[34:37]
	s_cbranch_vccnz .Lrestart1
.Lfast1:
	v_mfma_f32_16x16x32_f16 v[6:9], a[8:11], v[232:235], v[6:9]
	v_xor_b32_e32 v222, 0x4000, v222
	ds_read_b128 v[130:133], v222
	v_mfma_f32_16x16x32_f16 v[10:13], a[40:43], v[232:235], v[10:13]
	ds_read_b128 v[126:129], v222 offset:1024
	ds_read_b128 v[122:125], v222 offset:2048
	v_mfma_f32_16x16x32_f16 v[14:17], a[72:75], v[232:235], v[14:17]
	ds_read_b128 v[118:121], v222 offset:3072
	ds_read_b128 v[114:117], v222 offset:4096
	v_mfma_f32_16x16x32_f16 v[18:21], a[104:107], v[232:235], v[18:21]
	ds_read_b128 v[110:113], v222 offset:5120
	ds_read_b128 v[194:197], v222 offset:6144
	v_mfma_f32_16x16x32_f16 v[22:25], a[136:139], v[232:235], v[22:25]
	s_waitcnt vmcnt(1)
	v_mfma_f32_16x16x32_f16 v[26:29], a[168:171], v[232:235], v[26:29]
	v_bitop3_b32 v168, v70, v71, s30 bitop3:0x7e
	v_bitop3_b32 v169, v72, v73, s30 bitop3:0x7e
	v_mfma_f32_16x16x32_f16 v[30:33], a[200:203], v[232:235], v[30:33]
	v_bitop3_b32 v168, v168, v169, s18 bitop3:0xa8
	v_cmp_ne_u32_e32 vcc, 0, v168
	v_mfma_f32_16x16x32_f16 v[34:37], a[232:235], v[232:235], v[34:37]
	v_and_b32_e32 v240, v70, v167
	v_and_b32_e32 v241, v71, v167
	v_mfma_f32_16x16x32_f16 v[6:9], a[12:15], v[236:239], v[6:9]
	v_and_b32_e32 v242, v72, v167
	v_and_b32_e32 v243, v73, v167
	v_mfma_f32_16x16x32_f16 v[10:13], a[44:47], v[236:239], v[10:13]
	v_and_b32_dpp v244, v70, v167 row_ror:8 row_mask:0xf bank_mask:0xf
	v_and_b32_dpp v245, v71, v167 row_ror:8 row_mask:0xf bank_mask:0xf
	v_mfma_f32_16x16x32_f16 v[14:17], a[76:79], v[236:239], v[14:17]
	v_and_b32_dpp v246, v72, v167 row_ror:8 row_mask:0xf bank_mask:0xf
	v_and_b32_dpp v247, v73, v167 row_ror:8 row_mask:0xf bank_mask:0xf
	v_mfma_f32_16x16x32_f16 v[18:21], a[108:111], v[236:239], v[18:21]
	ds_read_b128 v[202:205], v222 offset:7168
	v_mfma_f32_16x16x32_f16 v[22:25], a[140:143], v[236:239], v[22:25]
	v_mfma_f32_16x16x32_f16 v[26:29], a[172:175], v[236:239], v[26:29]
	v_mfma_f32_16x16x32_f16 v[30:33], a[204:207], v[236:239], v[30:33]
	v_mfma_f32_16x16x32_f16 v[34:37], a[236:239], v[236:239], v[34:37]
	s_cbranch_vccnz .Lrestart2
.Lfast2:
	v_mfma_f32_16x16x32_f16 v[6:9], a[16:19], v[240:243], v[6:9]
	ds_read_b128 v[162:165], v222 offset:8192
	ds_read_b128 v[158:161], v222 offset:9216
	v_mfma_f32_16x16x32_f16 v[10:13], a[48:51], v[240:243], v[10:13]
	ds_read_b128 v[154:157], v222 offset:10240
	ds_read_b128 v[150:153], v222 offset:11264
	v_mfma_f32_16x16x32_f16 v[14:17], a[80:83], v[240:243], v[14:17]
	ds_read_b128 v[146:149], v222 offset:12288
	ds_read_b128 v[142:145], v222 offset:13312
	v_mfma_f32_16x16x32_f16 v[18:21], a[112:115], v[240:243], v[18:21]
	ds_read_b128 v[138:141], v222 offset:14336
	ds_read_b128 v[134:137], v222 offset:15360
	v_mfma_f32_16x16x32_f16 v[22:25], a[144:147], v[240:243], v[22:25]
	s_waitcnt vmcnt(0)
	v_mfma_f32_16x16x32_f16 v[26:29], a[176:179], v[240:243], v[26:29]
	v_bitop3_b32 v168, v74, v75, s30 bitop3:0x7e
	v_bitop3_b32 v169, v76, v77, s30 bitop3:0x7e
	v_mfma_f32_16x16x32_f16 v[30:33], a[208:211], v[240:243], v[30:33]
	v_bitop3_b32 v168, v168, v169, s18 bitop3:0xa8
	v_cmp_ne_u32_e32 vcc, 0, v168
	v_mfma_f32_16x16x32_f16 v[34:37], a[240:243], v[240:243], v[34:37]
	v_and_b32_e32 v248, v74, v167
	v_and_b32_e32 v249, v75, v167
	v_mfma_f32_16x16x32_f16 v[6:9], a[20:23], v[244:247], v[6:9]
	v_and_b32_e32 v250, v76, v167
	v_and_b32_e32 v251, v77, v167
	v_mfma_f32_16x16x32_f16 v[10:13], a[52:55], v[244:247], v[10:13]
	v_and_b32_dpp v252, v74, v167 row_ror:8 row_mask:0xf bank_mask:0xf
	v_and_b32_dpp v253, v75, v167 row_ror:8 row_mask:0xf bank_mask:0xf
	v_mfma_f32_16x16x32_f16 v[14:17], a[84:87], v[244:247], v[14:17]
	v_and_b32_dpp v254, v76, v167 row_ror:8 row_mask:0xf bank_mask:0xf
	v_and_b32_dpp v255, v77, v167 row_ror:8 row_mask:0xf bank_mask:0xf
	v_mfma_f32_16x16x32_f16 v[18:21], a[116:119], v[244:247], v[18:21]
	v_mfma_f32_16x16x32_f16 v[22:25], a[148:151], v[244:247], v[22:25]
	v_mfma_f32_16x16x32_f16 v[26:29], a[180:183], v[244:247], v[26:29]
	v_mfma_f32_16x16x32_f16 v[30:33], a[212:215], v[244:247], v[30:33]
	v_mfma_f32_16x16x32_f16 v[34:37], a[244:247], v[244:247], v[34:37]
	s_cbranch_vccnz .Lrestart3
.Lfast3:
	v_mfma_f32_16x16x32_f16 v[6:9], a[24:27], v[248:251], v[6:9]
	global_load_dwordx4 v[46:49], v[4:5], off
	v_mfma_f32_16x16x32_f16 v[10:13], a[56:59], v[248:251], v[10:13]
	global_load_dwordx4 v[50:53], v[4:5], off offset:16
	v_mfma_f32_16x16x32_f16 v[14:17], a[88:91], v[248:251], v[14:17]
	global_load_dwordx4 v[38:41], v[4:5], off offset:128
	v_mfma_f32_16x16x32_f16 v[18:21], a[120:123], v[248:251], v[18:21]
	global_load_dwordx4 v[42:45], v[4:5], off offset:144
	v_mfma_f32_16x16x32_f16 v[22:25], a[152:155], v[248:251], v[22:25]
	s_cmp_lg_u32 s31, 0
	s_cbranch_scc1 .Lno_warm
	global_load_dwordx4 v[54:57], v[172:173], off
	global_load_dwordx4 v[58:61], v[172:173], off offset:1024
.Lno_warm:
	v_mfma_f32_16x16x32_f16 v[26:29], a[184:187], v[248:251], v[26:29]
	v_mfma_f32_16x16x32_f16 v[30:33], a[216:219], v[248:251], v[30:33]
	v_mfma_f32_16x16x32_f16 v[34:37], a[248:251], v[248:251], v[34:37]
	v_mfma_f32_16x16x32_f16 v[6:9], a[28:31], v[252:255], v[6:9]
	v_mfma_f32_16x16x32_f16 v[10:13], a[60:63], v[252:255], v[10:13]
	v_mfma_f32_16x16x32_f16 v[14:17], a[92:95], v[252:255], v[14:17]
	v_mfma_f32_16x16x32_f16 v[18:21], a[124:127], v[252:255], v[18:21]
	v_mfma_f32_16x16x32_f16 v[22:25], a[156:159], v[252:255], v[22:25]
	v_mfma_f32_16x16x32_f16 v[26:29], a[188:191], v[252:255], v[26:29]
	v_mfma_f32_16x16x32_f16 v[30:33], a[220:223], v[252:255], v[30:33]
	v_mfma_f32_16x16x32_f16 v[34:37], a[252:255], v[252:255], v[34:37]

.Lrestart0:
	s_and_b64 vcc, exec, s[6:7]
	s_cbranch_vccnz .Lfast0
	s_add_i32 s17, s17, 1
	s_cmp_gt_u32 s17, 0x10000
	s_cselect_b64 s[6:7], -1, 0
	buffer_load_dwordx4 v[62:65], v78, s[8:11], s28 offen sc1
	buffer_load_dwordx4 v[66:69], v78, s[8:11], s28 offen offset:1024 sc1
	buffer_load_dwordx4 v[70:73], v78, s[8:11], s28 offen offset:2048 sc1
	buffer_load_dwordx4 v[74:77], v78, s[8:11], s28 offen offset:3072 sc1
	s_waitcnt vmcnt(3)
	v_bitop3_b32 v168, v62, v63, s30 bitop3:0x7e
	v_bitop3_b32 v169, v64, v65, s30 bitop3:0x7e
	v_bitop3_b32 v168, v168, v169, s18 bitop3:0xa8
	v_cmp_ne_u32_e32 vcc, 0, v168
	s_cbranch_vccnz .Lrestart0
	v_and_b32_e32 v224, v62, v167
	v_and_b32_e32 v225, v63, v167
	v_and_b32_e32 v226, v64, v167
	v_and_b32_e32 v227, v65, v167
	v_and_b32_dpp v228, v62, v167 row_ror:8 row_mask:0xf bank_mask:0xf
	v_and_b32_dpp v229, v63, v167 row_ror:8 row_mask:0xf bank_mask:0xf
	v_and_b32_dpp v230, v64, v167 row_ror:8 row_mask:0xf bank_mask:0xf
	v_and_b32_dpp v231, v65, v167 row_ror:8 row_mask:0xf bank_mask:0xf
	s_nop 1
	s_branch .Lfast0
.Lrestart1:
	s_and_b64 vcc, exec, s[6:7]
	s_cbranch_vccnz .Lfast1
	s_add_i32 s17, s17, 1
	s_cmp_gt_u32 s17, 0x10000
	s_cselect_b64 s[6:7], -1, 0
	buffer_load_dwordx4 v[66:69], v78, s[8:11], s28 offen offset:1024 sc1
	buffer_load_dwordx4 v[70:73], v78, s[8:11], s28 offen offset:2048 sc1
	buffer_load_dwordx4 v[74:77], v78, s[8:11], s28 offen offset:3072 sc1
	s_waitcnt vmcnt(2)
	v_bitop3_b32 v168, v66, v67, s30 bitop3:0x7e
	v_bitop3_b32 v169, v68, v69, s30 bitop3:0x7e
	v_bitop3_b32 v168, v168, v169, s18 bitop3:0xa8
	v_cmp_ne_u32_e32 vcc, 0, v168
	s_cbranch_vccnz .Lrestart1
	v_and_b32_e32 v232, v66, v167
	v_and_b32_e32 v233, v67, v167
	v_and_b32_e32 v234, v68, v167
	v_and_b32_e32 v235, v69, v167
	v_and_b32_dpp v236, v66, v167 row_ror:8 row_mask:0xf bank_mask:0xf
	v_and_b32_dpp v237, v67, v167 row_ror:8 row_mask:0xf bank_mask:0xf
	v_and_b32_dpp v238, v68, v167 row_ror:8 row_mask:0xf bank_mask:0xf
	v_and_b32_dpp v239, v69, v167 row_ror:8 row_mask:0xf bank_mask:0xf
	s_nop 1
	s_branch .Lfast1
.Lrestart2:
	s_and_b64 vcc, exec, s[6:7]
	s_cbranch_vccnz .Lfast2
	s_add_i32 s17, s17, 1
	s_cmp_gt_u32 s17, 0x10000
	s_cselect_b64 s[6:7], -1, 0
	buffer_load_dwordx4 v[70:73], v78, s[8:11], s28 offen offset:2048 sc1
	buffer_load_dwordx4 v[74:77], v78, s[8:11], s28 offen offset:3072 sc1
	s_waitcnt vmcnt(1)
	v_bitop3_b32 v168, v70, v71, s30 bitop3:0x7e
	v_bitop3_b32 v169, v72, v73, s30 bitop3:0x7e
	v_bitop3_b32 v168, v168, v169, s18 bitop3:0xa8
	v_cmp_ne_u32_e32 vcc, 0, v168
	s_cbranch_vccnz .Lrestart2
	v_and_b32_e32 v240, v70, v167
	v_and_b32_e32 v241, v71, v167
	v_and_b32_e32 v242, v72, v167
	v_and_b32_e32 v243, v73, v167
	v_and_b32_dpp v244, v70, v167 row_ror:8 row_mask:0xf bank_mask:0xf
	v_and_b32_dpp v245, v71, v167 row_ror:8 row_mask:0xf bank_mask:0xf
	v_and_b32_dpp v246, v72, v167 row_ror:8 row_mask:0xf bank_mask:0xf
	v_and_b32_dpp v247, v73, v167 row_ror:8 row_mask:0xf bank_mask:0xf
	s_nop 1
	s_branch .Lfast2
.Lrestart3:
	s_and_b64 vcc, exec, s[6:7]
	s_cbranch_vccnz .Lfast3
	s_add_i32 s17, s17, 1
	s_cmp_gt_u32 s17, 0x10000
	s_cselect_b64 s[6:7], -1, 0
	buffer_load_dwordx4 v[74:77], v78, s[8:11], s28 offen offset:3072 sc1
	s_waitcnt vmcnt(0)
	v_bitop3_b32 v168, v74, v75, s30 bitop3:0x7e
	v_bitop3_b32 v169, v76, v77, s30 bitop3:0x7e
	v_bitop3_b32 v168, v168, v169, s18 bitop3:0xa8
	v_cmp_ne_u32_e32 vcc, 0, v168
	s_cbranch_vccnz .Lrestart3
	v_and_b32_e32 v248, v74, v167
	v_and_b32_e32 v249, v75, v167
	v_and_b32_e32 v250, v76, v167
	v_and_b32_e32 v251, v77, v167
	v_and_b32_dpp v252, v74, v167 row_ror:8 row_mask:0xf bank_mask:0xf
	v_and_b32_dpp v253, v75, v167 row_ror:8 row_mask:0xf bank_mask:0xf
	v_and_b32_dpp v254, v76, v167 row_ror:8 row_mask:0xf bank_mask:0xf
	v_and_b32_dpp v255, v77, v167 row_ror:8 row_mask:0xf bank_mask:0xf
	s_nop 1
	s_branch .Lfast3
